# v22 + next-row prefetch (second register set) in the three non-router norm_phase row loops
# speedup vs baseline: 1.0001x; 1.0001x over previous
.LBB0_257:
	s_cmp_gt_i32 s96, 1
	s_cselect_b64 s[0:1], -1, 0
	s_cmp_lt_i32 s97, 2
	s_cselect_b64 s[2:3], -1, 0
	s_or_b64 s[0:1], s[0:1], s[2:3]
	s_and_b64 vcc, exec, s[0:1]
	s_cbranch_vccnz .LBB0_313
	v_readfirstlane_b32 s0, v0
	s_lshl_b32 s1, s8, 3
	s_lshr_b32 s0, s0, 6
	s_add_i32 s1, s0, s1
	s_ashr_i32 s12, s1, 1
	s_cmpk_gt_i32 s12, 0xfff
	s_cbranch_scc1 .LBB0_263
	s_and_b32 s5, s0, 1
	s_lshl_b32 s4, s9, 2
	s_mul_i32 s0, s5, 0xc000
	s_add_u32 s2, s94, s0
	s_addc_u32 s3, s95, 0
	s_waitcnt vmcnt(7)
	v_and_b32_e32 v35, 63, v0
	s_add_u32 s0, s2, 0x102000
	v_lshlrev_b32_e32 v34, 4, v35
	s_addc_u32 s1, s3, 0
	global_load_dwordx4 v[36:39], v34, s[0:1]
	global_load_dwordx4 v[40:43], v34, s[0:1] offset:1024
	global_load_dwordx4 v[44:47], v34, s[0:1] offset:2048
	global_load_dwordx4 v[48:51], v34, s[0:1] offset:3072
	v_mbcnt_lo_u32_b32 v2, -1, 0
	v_mbcnt_hi_u32_b32 v118, -1, v2
	v_and_b32_e32 v2, 64, v118
	v_readlane_b32 s52, v254, 2
	v_xor_b32_e32 v3, 1, v118
	v_add_u32_e32 v119, 64, v2
	v_or_b32_e32 v1, 0x1000, v34
	v_or_b32_e32 v22, 0x1400, v34
	v_or_b32_e32 v26, 0x1800, v34
	v_or_b32_e32 v30, 0x1c00, v34
	v_readlane_b32 s60, v254, 10
	v_readlane_b32 s61, v254, 11
	v_xor_b32_e32 v4, 2, v118
	v_cmp_lt_i32_e32 vcc, v3, v119
	s_add_u32 s2, s2, 0x100000
	global_load_dwordx4 v[52:55], v1, s[0:1]
	global_load_dwordx4 v[56:59], v22, s[0:1]
	global_load_dwordx4 v[60:63], v26, s[0:1]
	global_load_dwordx4 v[64:67], v30, s[0:1]
	global_load_dwordx4 v[68:71], v34, s[60:61]
	global_load_dwordx4 v[74:77], v34, s[60:61] offset:1024
	global_load_dwordx4 v[78:81], v34, s[60:61] offset:2048
	global_load_dwordx4 v[82:85], v34, s[60:61] offset:3072
	global_load_dwordx4 v[86:89], v1, s[60:61]
	global_load_dwordx4 v[90:93], v22, s[60:61]
	global_load_dwordx4 v[94:97], v26, s[60:61]
	global_load_dwordx4 v[98:101], v30, s[60:61]
	v_cndmask_b32_e32 v73, v118, v3, vcc
	v_cmp_lt_i32_e32 vcc, v4, v119
	s_addc_u32 s3, s3, 0
	v_xor_b32_e32 v72, 4, v118
	v_cndmask_b32_e32 v102, v118, v4, vcc
	global_load_dwordx4 v[2:5], v34, s[2:3]
	global_load_dwordx4 v[6:9], v34, s[2:3] offset:1024
	global_load_dwordx4 v[10:13], v34, s[2:3] offset:2048
	global_load_dwordx4 v[14:17], v34, s[2:3] offset:3072
	global_load_dwordx4 v[18:21], v1, s[2:3]
	s_nop 0
	global_load_dwordx4 v[22:25], v22, s[2:3]
	s_nop 0
	global_load_dwordx4 v[26:29], v26, s[2:3]
	s_nop 0
	global_load_dwordx4 v[30:33], v30, s[2:3]
	v_cmp_lt_i32_e32 vcc, v72, v119
	s_lshl_b32 s2, s5, 12
	s_add_i32 s2, s12, s2
	v_cndmask_b32_e32 v120, v118, v72, vcc
	v_lshlrev_b32_e32 v72, 2, v102
	s_ashr_i32 s3, s2, 31
	s_lshl_b64 s[6:7], s[2:3], 2
	s_add_u32 s13, s6, 0x2c0000
	s_addc_u32 s16, s7, 0
	s_ashr_i32 s5, s4, 31
	s_lshl_b64 s[10:11], s[2:3], 11
	s_lshl_b64 s[6:7], s[4:5], 2
	s_lshl_b64 s[2:3], s[2:3], 13
	v_readlane_b32 s53, v254, 3
	v_cmp_eq_u32_e64 s[0:1], 0, v35
	v_lshlrev_b32_e32 v1, 2, v73
	v_lshlrev_b32_e32 v73, 2, v120
	s_mov_b32 s17, 0x42fe0000
	s_mov_b32 s18, 0xc2fe0000
	s_mov_b32 s19, 0x4b400000
	s_mov_b32 s20, 0x40c0c00
	s_mov_b32 s21, 0x35200000
	v_readlane_b32 s54, v254, 4
	v_readlane_b32 s55, v254, 5
	v_readlane_b32 s56, v254, 6
	v_readlane_b32 s57, v254, 7
	v_readlane_b32 s58, v254, 8
	v_readlane_b32 s59, v254, 9
	v_readlane_b32 s62, v254, 12
	v_readlane_b32 s63, v254, 13
	v_readlane_b32 s64, v254, 14
	v_readlane_b32 s65, v254, 15
	v_readlane_b32 s66, v254, 16
	v_readlane_b32 s67, v254, 17
	s_waitcnt vmcnt(23)
	v_pk_add_f32 v[38:39], v[38:39], 1.0 op_sel_hi:[1,0]
	v_pk_add_f32 v[102:103], v[36:37], 1.0 op_sel_hi:[1,0]
	s_waitcnt vmcnt(22)
	v_pk_add_f32 v[42:43], v[42:43], 1.0 op_sel_hi:[1,0]
	v_pk_add_f32 v[104:105], v[40:41], 1.0 op_sel_hi:[1,0]
	s_waitcnt vmcnt(21)
	v_pk_add_f32 v[46:47], v[46:47], 1.0 op_sel_hi:[1,0]
	v_pk_add_f32 v[106:107], v[44:45], 1.0 op_sel_hi:[1,0]
	s_waitcnt vmcnt(20)
	v_pk_add_f32 v[50:51], v[50:51], 1.0 op_sel_hi:[1,0]
	v_pk_add_f32 v[108:109], v[48:49], 1.0 op_sel_hi:[1,0]
	s_waitcnt vmcnt(15)
	v_pk_mul_f32 v[36:37], v[70:71], v[38:39]
	v_pk_mul_f32 v[38:39], v[68:69], v[102:103]
	v_xor_b32_e32 v68, 8, v118
	v_cmp_lt_i32_e32 vcc, v68, v119
	s_waitcnt vmcnt(14)
	v_pk_mul_f32 v[40:41], v[76:77], v[42:43]
	v_pk_mul_f32 v[42:43], v[74:75], v[104:105]
	v_cndmask_b32_e32 v68, v118, v68, vcc
	v_lshlrev_b32_e32 v74, 2, v68
	v_xor_b32_e32 v68, 16, v118
	v_cmp_lt_i32_e32 vcc, v68, v119
	v_mov_b32_e32 v69, s11
	v_pk_add_f32 v[54:55], v[54:55], 1.0 op_sel_hi:[1,0]
	v_cndmask_b32_e32 v68, v118, v68, vcc
	v_lshlrev_b32_e32 v75, 2, v68
	v_xor_b32_e32 v68, 32, v118
	v_cmp_lt_i32_e32 vcc, v68, v119
	v_pk_add_f32 v[110:111], v[52:53], 1.0 op_sel_hi:[1,0]
	v_pk_add_f32 v[58:59], v[58:59], 1.0 op_sel_hi:[1,0]
	v_cndmask_b32_e32 v68, v118, v68, vcc
	v_lshlrev_b32_e32 v76, 2, v68
	v_lshl_or_b32 v68, v35, 2, s10
	s_lshl_b64 s[10:11], s[4:5], 11
	s_add_u32 s2, s52, s2
	v_mov_b32_e32 v35, 0
	s_addc_u32 s3, s53, s3
	v_pk_add_f32 v[112:113], v[56:57], 1.0 op_sel_hi:[1,0]
	v_pk_add_f32 v[62:63], v[62:63], 1.0 op_sel_hi:[1,0]
	v_pk_add_f32 v[114:115], v[60:61], 1.0 op_sel_hi:[1,0]
	v_pk_add_f32 v[66:67], v[66:67], 1.0 op_sel_hi:[1,0]
	v_pk_add_f32 v[116:117], v[64:65], 1.0 op_sel_hi:[1,0]
	v_lshl_add_u64 v[70:71], s[2:3], 0, v[34:35]
	s_mov_b64 s[2:3], 0x1000
	s_waitcnt vmcnt(13)
	v_pk_mul_f32 v[44:45], v[80:81], v[46:47]
	v_pk_mul_f32 v[46:47], v[78:79], v[106:107]
	s_waitcnt vmcnt(12)
	v_pk_mul_f32 v[48:49], v[84:85], v[50:51]
	v_pk_mul_f32 v[50:51], v[82:83], v[108:109]
	s_waitcnt vmcnt(11)
	v_pk_mul_f32 v[52:53], v[88:89], v[54:55]
	v_pk_mul_f32 v[54:55], v[86:87], v[110:111]
	s_waitcnt vmcnt(10)
	v_pk_mul_f32 v[56:57], v[92:93], v[58:59]
	v_pk_mul_f32 v[58:59], v[90:91], v[112:113]
	s_waitcnt vmcnt(9)
	v_pk_mul_f32 v[60:61], v[96:97], v[62:63]
	v_pk_mul_f32 v[62:63], v[94:95], v[114:115]
	s_waitcnt vmcnt(8)
	v_pk_mul_f32 v[64:65], v[100:101], v[66:67]
	v_pk_mul_f32 v[66:67], v[98:99], v[116:117]
	v_lshl_add_u64 v[70:71], v[70:71], 0, s[2:3]
	s_lshl_b64 s[14:15], s[4:5], 13
	v_mov_b32_e32 v34, 0x358637bd
	s_mov_b32 s5, 0xf800000
	v_mov_b32_e32 v77, 0x260
	v_mov_b32_e32 v78, 0x42fe0000
	global_load_dwordx4 v[150:153], v[70:71], off offset:-4096
	global_load_dwordx4 v[154:157], v[70:71], off offset:-3072
	global_load_dwordx4 v[158:161], v[70:71], off offset:-2048
	global_load_dwordx4 v[162:165], v[70:71], off offset:1024
	global_load_dwordx4 v[166:169], v[70:71], off
	global_load_dwordx4 v[170:173], v[70:71], off offset:-1024
	global_load_dwordx4 v[174:177], v[70:71], off offset:3072
	global_load_dwordx4 v[178:181], v[70:71], off offset:2048
	s_waitcnt vmcnt(0)
	s_branch .LrpN1_in

.LBB0_261:
	s_waitcnt vmcnt(8)
.LrpN1_in:
	v_mov_b32_e32 v80, v150
	v_mov_b32_e32 v81, v151
	v_mov_b32_e32 v82, v152
	v_mov_b32_e32 v83, v153
	v_mov_b32_e32 v84, v154
	v_mov_b32_e32 v85, v155
	v_mov_b32_e32 v86, v156
	v_mov_b32_e32 v87, v157
	v_mov_b32_e32 v88, v158
	v_mov_b32_e32 v89, v159
	v_mov_b32_e32 v90, v160
	v_mov_b32_e32 v91, v161
	v_mov_b32_e32 v92, v162
	v_mov_b32_e32 v93, v163
	v_mov_b32_e32 v94, v164
	v_mov_b32_e32 v95, v165
	v_mov_b32_e32 v96, v166
	v_mov_b32_e32 v97, v167
	v_mov_b32_e32 v98, v168
	v_mov_b32_e32 v99, v169
	v_mov_b32_e32 v100, v170
	v_mov_b32_e32 v101, v171
	v_mov_b32_e32 v102, v172
	v_mov_b32_e32 v103, v173
	v_mov_b32_e32 v104, v174
	v_mov_b32_e32 v105, v175
	v_mov_b32_e32 v106, v176
	v_mov_b32_e32 v107, v177
	v_mov_b32_e32 v108, v178
	v_mov_b32_e32 v109, v179
	v_mov_b32_e32 v110, v180
	v_mov_b32_e32 v111, v181
	s_add_i32 s22, s12, s4
	s_cmpk_lt_i32 s22, 0x1000
	s_cbranch_scc0 .LrpN1_np
	v_lshl_add_u64 v[146:147], v[70:71], 0, s[14:15]
	global_load_dwordx4 v[150:153], v[146:147], off offset:-4096
	global_load_dwordx4 v[154:157], v[146:147], off offset:-3072
	global_load_dwordx4 v[158:161], v[146:147], off offset:-2048
	global_load_dwordx4 v[162:165], v[146:147], off offset:1024
	global_load_dwordx4 v[166:169], v[146:147], off
	global_load_dwordx4 v[170:173], v[146:147], off offset:-1024
	global_load_dwordx4 v[174:177], v[146:147], off offset:3072
	global_load_dwordx4 v[178:181], v[146:147], off offset:2048
.LrpN1_np:
	v_mov_b32_e32 v114, v81
	v_mov_b32_e32 v115, v85
	v_pk_mul_f32 v[116:117], v[90:91], v[90:91]
	v_pk_mul_f32 v[118:119], v[88:89], v[88:89]
	v_pk_mul_f32 v[120:121], v[94:95], v[94:95]
	v_pk_mul_f32 v[122:123], v[92:93], v[92:93]
	v_mov_b32_e32 v126, v83
	v_mov_b32_e32 v127, v87
	v_mov_b32_e32 v112, v80
	v_mov_b32_e32 v113, v84
	v_mov_b32_e32 v124, v82
	v_mov_b32_e32 v125, v86
	v_pk_mov_b32 v[136:137], v[118:119], v[116:117] op_sel:[1,0]
	v_mov_b32_e32 v119, v117
	v_pk_mov_b32 v[116:117], v[122:123], v[120:121] op_sel:[1,0]
	v_mov_b32_e32 v123, v121
	v_pk_mul_f32 v[114:115], v[114:115], v[114:115]
	v_pk_mul_f32 v[120:121], v[126:127], v[126:127]
	v_pk_fma_f32 v[112:113], v[112:113], v[112:113], v[114:115]
	v_pk_fma_f32 v[114:115], v[124:125], v[124:125], v[120:121]
	v_mul_f32_e32 v128, v101, v101
	v_mul_f32_e32 v130, v103, v103
	v_pk_add_f32 v[118:119], v[136:137], v[118:119]
	v_pk_add_f32 v[112:113], v[112:113], v[114:115]
	v_mul_f32_e32 v79, v96, v96
	v_mul_f32_e32 v135, v97, v97
	v_mul_f32_e32 v138, v98, v98
	v_mul_f32_e32 v139, v99, v99
	v_pk_fma_f32 v[126:127], v[100:101], v[100:101], v[128:129] op_sel_hi:[1,1,0]
	v_pk_fma_f32 v[128:129], v[102:103], v[102:103], v[130:131] op_sel_hi:[1,1,0]
	v_pk_add_f32 v[118:119], v[118:119], v[118:119] op_sel:[0,1] op_sel_hi:[1,0]
	v_pk_add_f32 v[112:113], v[112:113], v[112:113] op_sel:[0,1] op_sel_hi:[1,0]
	v_mov_b32_e32 v127, v138
	v_mov_b32_e32 v129, v139
	v_mov_b32_e32 v119, v135
	v_mov_b32_e32 v113, v79
	v_pk_add_f32 v[114:115], v[126:127], v[128:129]
	v_pk_add_f32 v[112:113], v[112:113], v[118:119]
	v_mul_f32_e32 v132, v109, v109
	v_mul_f32_e32 v134, v111, v111
	v_pk_add_f32 v[116:117], v[116:117], v[122:123]
	v_pk_add_f32 v[112:113], v[112:113], v[114:115]
	v_mul_f32_e32 v140, v106, v106
	v_mul_f32_e32 v141, v107, v107
	v_mul_f32_e32 v142, v104, v104
	v_mul_f32_e32 v143, v105, v105
	v_pk_fma_f32 v[130:131], v[108:109], v[108:109], v[132:133] op_sel_hi:[1,1,0]
	v_pk_fma_f32 v[132:133], v[110:111], v[110:111], v[134:135] op_sel_hi:[1,1,0]
	v_pk_add_f32 v[116:117], v[116:117], v[116:117] op_sel:[0,1] op_sel_hi:[1,0]
	v_pk_add_f32 v[112:113], v[112:113], v[112:113] op_sel:[0,1] op_sel_hi:[1,0]
	v_mov_b32_e32 v131, v140
	v_mov_b32_e32 v133, v141
	v_mov_b32_e32 v117, v143
	v_mov_b32_e32 v113, v142
	v_pk_add_f32 v[120:121], v[130:131], v[132:133]
	v_pk_add_f32 v[112:113], v[112:113], v[116:117]
	s_nop 0
	v_pk_add_f32 v[112:113], v[112:113], v[120:121]
	s_nop 0
	v_add_f32_e32 v79, v112, v113
	ds_bpermute_b32 v112, v1, v79
	s_waitcnt lgkmcnt(0)
	v_add_f32_e32 v79, v79, v112
	ds_bpermute_b32 v112, v72, v79
	s_waitcnt lgkmcnt(0)
	v_add_f32_e32 v79, v79, v112
	ds_bpermute_b32 v112, v73, v79
	s_waitcnt lgkmcnt(0)
	v_add_f32_e32 v79, v79, v112
	ds_bpermute_b32 v112, v74, v79
	s_waitcnt lgkmcnt(0)
	v_add_f32_e32 v79, v79, v112
	ds_bpermute_b32 v112, v75, v79
	s_waitcnt lgkmcnt(0)
	v_add_f32_e32 v79, v79, v112
	ds_bpermute_b32 v112, v76, v79
	s_waitcnt lgkmcnt(0)
	v_add_f32_e32 v79, v79, v112
	v_fmamk_f32 v79, v79, 0x3a000000, v34
	v_mul_f32_e32 v112, 0x4f800000, v79
	v_cmp_gt_f32_e32 vcc, s5, v79
	s_nop 1
	v_cndmask_b32_e32 v79, v79, v112, vcc
	v_sqrt_f32_e32 v112, v79
	s_nop 0
	v_add_u32_e32 v113, -1, v112
	v_add_u32_e32 v114, 1, v112
	v_fma_f32 v115, -v113, v112, v79
	v_fma_f32 v116, -v114, v112, v79
	v_cmp_ge_f32_e64 s[2:3], 0, v115
	s_nop 1
	v_cndmask_b32_e64 v112, v112, v113, s[2:3]
	v_cmp_lt_f32_e64 s[2:3], 0, v116
	s_nop 1
	v_cndmask_b32_e64 v112, v112, v114, s[2:3]
	v_mul_f32_e32 v113, 0x37800000, v112
	v_cndmask_b32_e32 v112, v112, v113, vcc
	v_cmp_class_f32_e32 vcc, v79, v77
	s_nop 1
	v_cndmask_b32_e32 v79, v112, v79, vcc
	v_div_scale_f32 v112, s[2:3], v79, v79, 1.0
	v_rcp_f32_e32 v113, v112
	v_div_scale_f32 v114, vcc, 1.0, v79, 1.0
	v_fma_f32 v115, -v112, v113, 1.0
	v_fmac_f32_e32 v113, v115, v113
	v_mul_f32_e32 v115, v114, v113
	v_fma_f32 v116, -v112, v115, v114
	v_fmac_f32_e32 v115, v116, v113
	v_fma_f32 v112, -v112, v115, v114
	v_div_fmas_f32 v112, v112, v113, v115
	v_div_fixup_f32 v112, v112, v79, 1.0
	v_pk_mul_f32 v[80:81], v[80:81], v[112:113] op_sel_hi:[1,0]
	v_pk_mul_f32 v[82:83], v[82:83], v[112:113] op_sel_hi:[1,0]
	v_pk_mul_f32 v[84:85], v[84:85], v[112:113] op_sel_hi:[1,0]
	v_pk_mul_f32 v[86:87], v[86:87], v[112:113] op_sel_hi:[1,0]
	v_pk_fma_f32 v[82:83], v[36:37], v[82:83], v[4:5]
	v_pk_fma_f32 v[80:81], v[38:39], v[80:81], v[2:3]
	v_pk_mul_f32 v[88:89], v[88:89], v[112:113] op_sel_hi:[1,0]
	v_pk_mul_f32 v[90:91], v[90:91], v[112:113] op_sel_hi:[1,0]
	v_pk_mul_f32 v[100:101], v[100:101], v[112:113] op_sel_hi:[1,0]
	v_pk_mul_f32 v[102:103], v[102:103], v[112:113] op_sel_hi:[1,0]
	v_pk_mul_f32 v[96:97], v[96:97], v[112:113] op_sel_hi:[1,0]
	v_pk_mul_f32 v[98:99], v[98:99], v[112:113] op_sel_hi:[1,0]
	v_pk_mul_f32 v[92:93], v[92:93], v[112:113] op_sel_hi:[1,0]
	v_pk_mul_f32 v[94:95], v[94:95], v[112:113] op_sel_hi:[1,0]
	v_pk_mul_f32 v[108:109], v[108:109], v[112:113] op_sel_hi:[1,0]
	v_pk_mul_f32 v[110:111], v[110:111], v[112:113] op_sel_hi:[1,0]
	v_pk_mul_f32 v[104:105], v[104:105], v[112:113] op_sel_hi:[1,0]
	v_pk_mul_f32 v[106:107], v[106:107], v[112:113] op_sel_hi:[1,0]
	v_pk_fma_f32 v[86:87], v[40:41], v[86:87], v[8:9]
	v_pk_fma_f32 v[84:85], v[42:43], v[84:85], v[6:7]
	v_max_f32_e64 v79, |v80|, |v81|
	v_max_f32_e64 v112, |v82|, |v83|
	v_pk_fma_f32 v[90:91], v[44:45], v[90:91], v[12:13]
	v_pk_fma_f32 v[88:89], v[46:47], v[88:89], v[10:11]
	v_max_f32_e64 v113, |v84|, |v85|
	v_max_f32_e64 v114, |v86|, |v87|
	v_max3_f32 v79, v79, 0, v112
	v_pk_fma_f32 v[102:103], v[48:49], v[102:103], v[16:17]
	v_pk_fma_f32 v[100:101], v[50:51], v[100:101], v[14:15]
	v_max_f32_e64 v115, |v88|, |v89|
	v_max_f32_e64 v116, |v90|, |v91|
	v_max3_f32 v79, v79, v113, v114
	v_pk_fma_f32 v[98:99], v[52:53], v[98:99], v[20:21]
	v_pk_fma_f32 v[96:97], v[54:55], v[96:97], v[18:19]
	v_max_f32_e64 v117, |v100|, |v101|
	v_max_f32_e64 v118, |v102|, |v103|
	v_max3_f32 v79, v79, v115, v116
	v_pk_fma_f32 v[94:95], v[56:57], v[94:95], v[24:25]
	v_pk_fma_f32 v[92:93], v[58:59], v[92:93], v[22:23]
	v_max_f32_e64 v119, |v96|, |v97|
	v_max_f32_e64 v120, |v98|, |v99|
	v_max3_f32 v79, v79, v117, v118
	v_pk_fma_f32 v[110:111], v[60:61], v[110:111], v[28:29]
	v_pk_fma_f32 v[108:109], v[62:63], v[108:109], v[26:27]
	v_max_f32_e64 v121, |v92|, |v93|
	v_max_f32_e64 v122, |v94|, |v95|
	v_max3_f32 v79, v79, v119, v120
	v_pk_fma_f32 v[106:107], v[64:65], v[106:107], v[32:33]
	v_pk_fma_f32 v[104:105], v[66:67], v[104:105], v[30:31]
	v_max_f32_e64 v123, |v108|, |v109|
	v_max_f32_e64 v124, |v110|, |v111|
	v_max3_f32 v79, v79, v121, v122
	v_max_f32_e64 v125, |v104|, |v105|
	v_max_f32_e64 v126, |v106|, |v107|
	v_max3_f32 v79, v79, v123, v124
	v_max3_f32 v79, v79, v125, v126
	ds_bpermute_b32 v112, v1, v79
	s_waitcnt lgkmcnt(0)
	v_max_f32_e32 v112, v112, v112
	v_max_f32_e32 v79, v79, v112
	ds_bpermute_b32 v112, v72, v79
	s_waitcnt lgkmcnt(0)
	v_max_f32_e32 v112, v112, v112
	v_max_f32_e32 v79, v79, v112
	ds_bpermute_b32 v112, v73, v79
	s_waitcnt lgkmcnt(0)
	v_max_f32_e32 v112, v112, v112
	v_max_f32_e32 v79, v79, v112
	ds_bpermute_b32 v112, v74, v79
	s_waitcnt lgkmcnt(0)
	v_max_f32_e32 v112, v112, v112
	v_max_f32_e32 v79, v79, v112
	ds_bpermute_b32 v112, v75, v79
	s_waitcnt lgkmcnt(0)
	v_max_f32_e32 v112, v112, v112
	v_max_f32_e32 v79, v79, v112
	ds_bpermute_b32 v114, v76, v79
	v_lshl_add_u64 v[112:113], s[94:95], 0, v[68:69]
	v_add_co_u32_e32 v112, vcc, s21, v112
	s_waitcnt lgkmcnt(0)
	v_max_f32_e32 v114, v114, v114
	v_max_f32_e32 v79, v79, v114
	v_div_scale_f32 v114, s[2:3], v79, v79, s17
	v_rcp_f32_e32 v115, v114
	v_addc_co_u32_e32 v113, vcc, 0, v113, vcc
	v_div_scale_f32 v116, vcc, s17, v79, s17
	v_fma_f32 v117, -v114, v115, 1.0
	v_fmac_f32_e32 v115, v117, v115
	v_mul_f32_e32 v117, v116, v115
	v_fma_f32 v118, -v114, v117, v116
	v_fmac_f32_e32 v117, v118, v115
	v_fma_f32 v114, -v114, v117, v116
	v_div_fmas_f32 v114, v114, v115, v117
	v_div_fixup_f32 v114, v114, v79, s17
	v_cmp_lt_f32_e32 vcc, 0, v79
	s_nop 1
	v_cndmask_b32_e32 v114, 0, v114, vcc
	v_mul_f32_e32 v81, v81, v114
	v_mul_f32_e32 v80, v80, v114
	v_mul_f32_e32 v82, v82, v114
	v_mul_f32_e32 v83, v83, v114
	v_med3_f32 v81, v81, s18, v78
	v_med3_f32 v80, v80, s18, v78
	v_med3_f32 v82, v82, s18, v78
	v_med3_f32 v83, v83, s18, v78
	v_add_f32_e32 v81, 0x4b400000, v81
	v_add_f32_e32 v80, 0x4b400000, v80
	v_add_f32_sdwa v82, v82, s19 dst_sel:WORD_1 dst_unused:UNUSED_PAD src0_sel:DWORD src1_sel:DWORD
	v_add_f32_e32 v83, 0x4b400000, v83
	v_lshlrev_b32_e32 v81, 8, v81
	v_mul_f32_e32 v85, v85, v114
	v_and_b32_e32 v82, 0xff0000, v82
	v_perm_b32 v80, v83, v80, s20
	v_and_b32_e32 v81, 0xff00, v81
	v_mul_f32_e32 v84, v84, v114
	v_mul_f32_e32 v86, v86, v114
	v_mul_f32_e32 v87, v87, v114
	v_med3_f32 v85, v85, s18, v78
	v_or3_b32 v80, v80, v81, v82
	v_med3_f32 v84, v84, s18, v78
	v_add_f32_e32 v85, 0x4b400000, v85
	global_store_dword v[112:113], v80, off
	v_med3_f32 v80, v86, s18, v78
	v_med3_f32 v81, v87, s18, v78
	v_add_f32_e32 v84, 0x4b400000, v84
	v_add_f32_sdwa v80, v80, s19 dst_sel:WORD_1 dst_unused:UNUSED_PAD src0_sel:DWORD src1_sel:DWORD
	v_add_f32_e32 v81, 0x4b400000, v81
	v_lshlrev_b32_e32 v82, 8, v85
	v_and_b32_e32 v82, 0xff00, v82
	v_and_b32_e32 v80, 0xff0000, v80
	v_perm_b32 v81, v81, v84, s20
	v_or3_b32 v80, v81, v82, v80
	v_mul_f32_e32 v81, v89, v114
	global_store_dword v[112:113], v80, off offset:256
	v_mul_f32_e32 v80, v88, v114
	v_mul_f32_e32 v82, v90, v114
	v_mul_f32_e32 v83, v91, v114
	v_med3_f32 v81, v81, s18, v78
	v_med3_f32 v80, v80, s18, v78
	v_add_f32_e32 v81, 0x4b400000, v81
	v_med3_f32 v82, v82, s18, v78
	v_med3_f32 v83, v83, s18, v78
	v_add_f32_e32 v80, 0x4b400000, v80
	v_add_f32_sdwa v82, v82, s19 dst_sel:WORD_1 dst_unused:UNUSED_PAD src0_sel:DWORD src1_sel:DWORD
	v_add_f32_e32 v83, 0x4b400000, v83
	v_lshlrev_b32_e32 v81, 8, v81
	v_and_b32_e32 v81, 0xff00, v81
	v_and_b32_e32 v82, 0xff0000, v82
	v_perm_b32 v80, v83, v80, s20
	v_or3_b32 v80, v80, v81, v82
	v_mul_f32_e32 v81, v101, v114
	global_store_dword v[112:113], v80, off offset:512
	v_mul_f32_e32 v80, v100, v114
	v_mul_f32_e32 v82, v102, v114
	v_mul_f32_e32 v83, v103, v114
	v_med3_f32 v81, v81, s18, v78
	v_med3_f32 v80, v80, s18, v78
	v_add_f32_e32 v81, 0x4b400000, v81
	v_med3_f32 v82, v82, s18, v78
	v_med3_f32 v83, v83, s18, v78
	v_add_f32_e32 v80, 0x4b400000, v80
	v_add_f32_sdwa v82, v82, s19 dst_sel:WORD_1 dst_unused:UNUSED_PAD src0_sel:DWORD src1_sel:DWORD
	v_add_f32_e32 v83, 0x4b400000, v83
	v_lshlrev_b32_e32 v81, 8, v81
	v_and_b32_e32 v81, 0xff00, v81
	v_and_b32_e32 v82, 0xff0000, v82
	v_perm_b32 v80, v83, v80, s20
	v_or3_b32 v80, v80, v81, v82
	v_mul_f32_e32 v81, v97, v114
	global_store_dword v[112:113], v80, off offset:768
	v_mul_f32_e32 v80, v96, v114
	v_mul_f32_e32 v82, v98, v114
	v_mul_f32_e32 v83, v99, v114
	v_med3_f32 v81, v81, s18, v78
	v_med3_f32 v80, v80, s18, v78
	v_add_f32_e32 v81, 0x4b400000, v81
	v_med3_f32 v82, v82, s18, v78
	v_med3_f32 v83, v83, s18, v78
	v_add_f32_e32 v80, 0x4b400000, v80
	v_add_f32_sdwa v82, v82, s19 dst_sel:WORD_1 dst_unused:UNUSED_PAD src0_sel:DWORD src1_sel:DWORD
	v_add_f32_e32 v83, 0x4b400000, v83
	v_lshlrev_b32_e32 v81, 8, v81
	v_and_b32_e32 v81, 0xff00, v81
	v_and_b32_e32 v82, 0xff0000, v82
	v_perm_b32 v80, v83, v80, s20
	v_or3_b32 v80, v80, v81, v82
	v_mul_f32_e32 v81, v93, v114
	global_store_dword v[112:113], v80, off offset:1024
	v_mul_f32_e32 v80, v92, v114
	v_mul_f32_e32 v82, v94, v114
	v_mul_f32_e32 v83, v95, v114
	v_med3_f32 v81, v81, s18, v78
	v_med3_f32 v80, v80, s18, v78
	v_add_f32_e32 v81, 0x4b400000, v81
	v_med3_f32 v82, v82, s18, v78
	v_med3_f32 v83, v83, s18, v78
	v_add_f32_e32 v80, 0x4b400000, v80
	v_add_f32_sdwa v82, v82, s19 dst_sel:WORD_1 dst_unused:UNUSED_PAD src0_sel:DWORD src1_sel:DWORD
	v_add_f32_e32 v83, 0x4b400000, v83
	v_lshlrev_b32_e32 v81, 8, v81
	v_and_b32_e32 v81, 0xff00, v81
	v_and_b32_e32 v82, 0xff0000, v82
	v_perm_b32 v80, v83, v80, s20
	v_or3_b32 v80, v80, v81, v82
	v_mul_f32_e32 v81, v109, v114
	global_store_dword v[112:113], v80, off offset:1280
	v_mul_f32_e32 v80, v108, v114
	v_mul_f32_e32 v82, v110, v114
	v_mul_f32_e32 v83, v111, v114
	v_med3_f32 v81, v81, s18, v78
	v_med3_f32 v80, v80, s18, v78
	v_add_f32_e32 v81, 0x4b400000, v81
	v_med3_f32 v82, v82, s18, v78
	v_med3_f32 v83, v83, s18, v78
	v_add_f32_e32 v80, 0x4b400000, v80
	v_add_f32_sdwa v82, v82, s19 dst_sel:WORD_1 dst_unused:UNUSED_PAD src0_sel:DWORD src1_sel:DWORD
	v_add_f32_e32 v83, 0x4b400000, v83
	v_lshlrev_b32_e32 v81, 8, v81
	v_and_b32_e32 v81, 0xff00, v81
	v_and_b32_e32 v82, 0xff0000, v82
	v_perm_b32 v80, v83, v80, s20
	v_or3_b32 v80, v80, v81, v82
	v_mul_f32_e32 v81, v105, v114
	global_store_dword v[112:113], v80, off offset:1536
	v_mul_f32_e32 v80, v104, v114
	v_mul_f32_e32 v82, v106, v114
	v_mul_f32_e32 v83, v107, v114
	v_med3_f32 v81, v81, s18, v78
	v_med3_f32 v80, v80, s18, v78
	v_add_f32_e32 v81, 0x4b400000, v81
	v_med3_f32 v82, v82, s18, v78
	v_med3_f32 v83, v83, s18, v78
	v_add_f32_e32 v80, 0x4b400000, v80
	v_add_f32_sdwa v82, v82, s19 dst_sel:WORD_1 dst_unused:UNUSED_PAD src0_sel:DWORD src1_sel:DWORD
	v_add_f32_e32 v83, 0x4b400000, v83
	v_lshlrev_b32_e32 v81, 8, v81
	v_and_b32_e32 v81, 0xff00, v81
	v_and_b32_e32 v82, 0xff0000, v82
	v_perm_b32 v80, v83, v80, s20
	v_or3_b32 v80, v80, v81, v82
	global_store_dword v[112:113], v80, off offset:1792
	s_and_saveexec_b64 s[2:3], s[0:1]
	s_cbranch_execz .LBB0_260
	s_add_u32 s22, s94, s13
	s_addc_u32 s23, s95, s16
	v_mul_f32_e32 v79, 0x3c010204, v79
	global_store_dword v35, v79, s[22:23]
	s_branch .LBB0_260

.LBB0_1430:
	s_cmp_gt_i32 s96, 7
	s_cselect_b64 s[0:1], -1, 0
	s_cmp_lt_i32 s97, 8
	s_cselect_b64 s[2:3], -1, 0
	s_or_b64 s[0:1], s[0:1], s[2:3]
	s_and_b64 vcc, exec, s[0:1]
	s_cbranch_vccnz .LBB0_1486
	v_readfirstlane_b32 s0, v0
	s_lshr_b32 s0, s0, 6
	s_lshl_b32 s1, s8, 3
	s_add_i32 s1, s0, s1
	s_ashr_i32 s10, s1, 1
	s_cmpk_gt_i32 s10, 0xfff
	s_cbranch_scc1 .LBB0_1436
	s_and_b32 s2, s0, 1
	s_mul_i32 s0, s2, 0xc000
	s_add_u32 s3, s94, s0
	s_addc_u32 s4, s95, 0
	s_waitcnt vmcnt(15)
	v_mov_b32_e32 v2, 0x1c00
	v_and_b32_e32 v116, 63, v0
	s_add_u32 s0, s3, 0x108000
	s_waitcnt vmcnt(8)
	v_lshl_or_b32 v30, v0, 4, v2
	v_mbcnt_lo_u32_b32 v2, -1, 0
	s_addc_u32 s1, s4, 0
	v_lshlrev_b32_e32 v1, 4, v116
	v_readlane_b32 s16, v254, 2
	v_mbcnt_hi_u32_b32 v117, -1, v2
	global_load_dwordx4 v[34:37], v1, s[0:1]
	global_load_dwordx4 v[38:41], v1, s[0:1] offset:1024
	global_load_dwordx4 v[42:45], v1, s[0:1] offset:2048
	v_or_b32_e32 v18, 0x1000, v1
	v_or_b32_e32 v22, 0x1400, v1
	v_or_b32_e32 v26, 0x1800, v1
	v_readlane_b32 s17, v254, 3
	v_readlane_b32 s18, v254, 4
	v_readlane_b32 s19, v254, 5
	v_readlane_b32 s20, v254, 6
	v_readlane_b32 s21, v254, 7
	v_readlane_b32 s22, v254, 8
	v_readlane_b32 s23, v254, 9
	v_readlane_b32 s24, v254, 10
	v_readlane_b32 s25, v254, 11
	v_and_b32_e32 v2, 64, v117
	global_load_dwordx4 v[46:49], v1, s[0:1] offset:3072
	global_load_dwordx4 v[50:53], v18, s[0:1]
	global_load_dwordx4 v[54:57], v22, s[0:1]
	global_load_dwordx4 v[58:61], v26, s[0:1]
	global_load_dwordx4 v[62:65], v30, s[0:1]
	v_readlane_b32 s26, v254, 12
	v_readlane_b32 s27, v254, 13
	v_readlane_b32 s28, v254, 14
	v_readlane_b32 s29, v254, 15
	v_readlane_b32 s30, v254, 16
	v_readlane_b32 s31, v254, 17
	s_mov_b64 s[16:17], s[24:25]
	v_xor_b32_e32 v3, 1, v117
	v_add_u32_e32 v118, 64, v2
	s_add_u32 s0, s3, 0x106000
	s_mov_b64 s[18:19], s[26:27]
	v_cmp_lt_i32_e32 vcc, v3, v118
	s_addc_u32 s1, s4, 0
	global_load_dwordx4 v[66:69], v1, s[18:19]
	global_load_dwordx4 v[72:75], v1, s[18:19] offset:1024
	global_load_dwordx4 v[76:79], v1, s[18:19] offset:2048
	global_load_dwordx4 v[80:83], v1, s[18:19] offset:3072
	global_load_dwordx4 v[84:87], v18, s[18:19]
	global_load_dwordx4 v[88:91], v22, s[18:19]
	global_load_dwordx4 v[92:95], v26, s[18:19]
	global_load_dwordx4 v[96:99], v30, s[18:19]
	v_cndmask_b32_e32 v100, v117, v3, vcc
	global_load_dwordx4 v[2:5], v1, s[0:1]
	global_load_dwordx4 v[6:9], v1, s[0:1] offset:1024
	global_load_dwordx4 v[10:13], v1, s[0:1] offset:2048
	global_load_dwordx4 v[14:17], v1, s[0:1] offset:3072
	s_nop 0
	global_load_dwordx4 v[18:21], v18, s[0:1]
	s_nop 0
	global_load_dwordx4 v[22:25], v22, s[0:1]
	s_nop 0
	global_load_dwordx4 v[26:29], v26, s[0:1]
	s_nop 0
	global_load_dwordx4 v[30:33], v30, s[0:1]
	v_xor_b32_e32 v70, 2, v117
	v_xor_b32_e32 v71, 4, v117
	v_cmp_lt_i32_e32 vcc, v70, v118
	v_lshlrev_b32_e32 v1, 2, v100
	s_lshl_b32 s2, s2, 12
	v_cndmask_b32_e32 v70, v117, v70, vcc
	v_cmp_lt_i32_e32 vcc, v71, v118
	s_add_i32 s2, s10, s2
	s_ashr_i32 s3, s2, 31
	v_cndmask_b32_e32 v71, v117, v71, vcc
	s_lshl_b32 s4, s9, 2
	s_lshl_b64 s[6:7], s[2:3], 2
	s_add_u32 s11, s6, 0x280000
	s_mov_b64 s[20:21], s[28:29]
	s_addc_u32 s16, s7, 0
	s_ashr_i32 s5, s4, 31
	s_lshl_b64 s[12:13], s[2:3], 11
	s_lshl_b64 s[2:3], s[2:3], 12
	v_lshlrev_b32_e32 v70, 2, v70
	v_lshlrev_b32_e32 v71, 2, v71
	v_cmp_eq_u32_e64 s[0:1], 0, v116
	s_lshl_b64 s[6:7], s[4:5], 2
	s_lshl_b64 s[34:35], s[4:5], 12
	s_mov_b32 s17, 0x42fe0000
	s_mov_b32 s18, 0xc2fe0000
	s_mov_b32 s19, 0x4b400000
	s_mov_b32 s20, 0x40c0c00
	s_mov_b32 s21, 0x6e600000
	s_mov_b64 s[22:23], s[30:31]
	s_waitcnt vmcnt(23)
	v_pk_add_f32 v[36:37], v[36:37], 1.0 op_sel_hi:[1,0]
	v_pk_add_f32 v[100:101], v[34:35], 1.0 op_sel_hi:[1,0]
	s_waitcnt vmcnt(22)
	v_pk_add_f32 v[40:41], v[40:41], 1.0 op_sel_hi:[1,0]
	v_pk_add_f32 v[102:103], v[38:39], 1.0 op_sel_hi:[1,0]
	s_waitcnt vmcnt(21)
	v_pk_add_f32 v[44:45], v[44:45], 1.0 op_sel_hi:[1,0]
	v_pk_add_f32 v[104:105], v[42:43], 1.0 op_sel_hi:[1,0]
	s_waitcnt vmcnt(20)
	v_pk_add_f32 v[48:49], v[48:49], 1.0 op_sel_hi:[1,0]
	v_pk_add_f32 v[106:107], v[46:47], 1.0 op_sel_hi:[1,0]
	s_waitcnt vmcnt(19)
	v_pk_add_f32 v[52:53], v[52:53], 1.0 op_sel_hi:[1,0]
	v_pk_add_f32 v[108:109], v[50:51], 1.0 op_sel_hi:[1,0]
	s_waitcnt vmcnt(18)
	v_pk_add_f32 v[56:57], v[56:57], 1.0 op_sel_hi:[1,0]
	v_pk_add_f32 v[110:111], v[54:55], 1.0 op_sel_hi:[1,0]
	s_waitcnt vmcnt(17)
	v_pk_add_f32 v[60:61], v[60:61], 1.0 op_sel_hi:[1,0]
	v_pk_add_f32 v[112:113], v[58:59], 1.0 op_sel_hi:[1,0]
	s_waitcnt vmcnt(16)
	v_pk_add_f32 v[64:65], v[64:65], 1.0 op_sel_hi:[1,0]
	v_pk_add_f32 v[114:115], v[62:63], 1.0 op_sel_hi:[1,0]
	s_waitcnt vmcnt(15)
	v_pk_mul_f32 v[34:35], v[68:69], v[36:37]
	v_pk_mul_f32 v[36:37], v[66:67], v[100:101]
	v_xor_b32_e32 v66, 8, v117
	v_cmp_lt_i32_e32 vcc, v66, v118
	s_waitcnt vmcnt(14)
	v_pk_mul_f32 v[38:39], v[74:75], v[40:41]
	v_pk_mul_f32 v[40:41], v[72:73], v[102:103]
	v_cndmask_b32_e32 v66, v117, v66, vcc
	v_lshlrev_b32_e32 v72, 2, v66
	v_xor_b32_e32 v66, 16, v117
	v_cmp_lt_i32_e32 vcc, v66, v118
	s_waitcnt vmcnt(13)
	v_pk_mul_f32 v[42:43], v[78:79], v[44:45]
	v_pk_mul_f32 v[44:45], v[76:77], v[104:105]
	v_cndmask_b32_e32 v66, v117, v66, vcc
	v_lshlrev_b32_e32 v73, 2, v66
	v_xor_b32_e32 v66, 32, v117
	v_cmp_lt_i32_e32 vcc, v66, v118
	s_waitcnt vmcnt(12)
	v_pk_mul_f32 v[46:47], v[82:83], v[48:49]
	v_pk_mul_f32 v[48:49], v[80:81], v[106:107]
	v_cndmask_b32_e32 v66, v117, v66, vcc
	s_waitcnt vmcnt(11)
	v_pk_mul_f32 v[50:51], v[86:87], v[52:53]
	v_pk_mul_f32 v[52:53], v[84:85], v[108:109]
	s_waitcnt vmcnt(10)
	v_pk_mul_f32 v[54:55], v[90:91], v[56:57]
	v_pk_mul_f32 v[56:57], v[88:89], v[110:111]
	s_waitcnt vmcnt(9)
	v_pk_mul_f32 v[58:59], v[94:95], v[60:61]
	v_pk_mul_f32 v[60:61], v[92:93], v[112:113]
	s_waitcnt vmcnt(8)
	v_pk_mul_f32 v[62:63], v[98:99], v[64:65]
	v_pk_mul_f32 v[64:65], v[96:97], v[114:115]
	v_lshlrev_b32_e32 v74, 2, v66
	v_lshl_or_b32 v66, v116, 2, s12
	v_mov_b32_e32 v67, s13
	s_lshl_b64 s[12:13], s[4:5], 11
	v_lshl_or_b32 v68, v116, 3, s2
	v_mov_b32_e32 v69, s3
	v_mov_b32_e32 v75, 0x358637bd
	s_mov_b32 s5, 0xf800000
	v_mov_b32_e32 v76, 0x260
	v_mov_b32_e32 v77, 0
	v_mov_b32_e32 v78, 0x42fe0000
	v_lshl_add_u64 v[150:151], s[94:95], 0, v[68:69]
	v_add_co_u32_e32 v150, vcc, 0x48200000, v150
	s_nop 1
	v_addc_co_u32_e32 v151, vcc, 0, v151, vcc
	global_load_dwordx2 v[152:153], v[150:151], off
	global_load_dwordx2 v[154:155], v[150:151], off offset:512
	global_load_dwordx2 v[156:157], v[150:151], off offset:1024
	global_load_dwordx2 v[158:159], v[150:151], off offset:1536
	global_load_dwordx2 v[160:161], v[150:151], off offset:2048
	global_load_dwordx2 v[162:163], v[150:151], off offset:2560
	global_load_dwordx2 v[164:165], v[150:151], off offset:3072
	s_nop 0
	global_load_dwordx2 v[150:151], v[150:151], off offset:3584
	s_waitcnt vmcnt(0)
	s_branch .LrpN2_in

.LrpN2_in:
	v_mov_b32_e32 v80, v150
	v_mov_b32_e32 v81, v151
	v_mov_b32_e32 v82, v152
	v_mov_b32_e32 v83, v153
	v_mov_b32_e32 v84, v154
	v_mov_b32_e32 v85, v155
	v_mov_b32_e32 v86, v156
	v_mov_b32_e32 v87, v157
	v_mov_b32_e32 v88, v158
	v_mov_b32_e32 v89, v159
	v_mov_b32_e32 v90, v160
	v_mov_b32_e32 v91, v161
	v_mov_b32_e32 v92, v162
	v_mov_b32_e32 v93, v163
	v_mov_b32_e32 v94, v164
	v_mov_b32_e32 v95, v165
	s_add_i32 s22, s10, s4
	s_cmpk_lt_i32 s22, 0x1000
	s_cbranch_scc0 .LrpN2_np
	v_lshl_add_u64 v[146:147], v[68:69], 0, s[34:35]
	v_lshl_add_u64 v[150:151], s[94:95], 0, v[146:147]
	v_add_co_u32_e32 v150, vcc, 0x48200000, v150
	s_nop 1
	v_addc_co_u32_e32 v151, vcc, 0, v151, vcc
	global_load_dwordx2 v[152:153], v[150:151], off
	global_load_dwordx2 v[154:155], v[150:151], off offset:512
	global_load_dwordx2 v[156:157], v[150:151], off offset:1024
	global_load_dwordx2 v[158:159], v[150:151], off offset:1536
	global_load_dwordx2 v[160:161], v[150:151], off offset:2048
	global_load_dwordx2 v[162:163], v[150:151], off offset:2560
	global_load_dwordx2 v[164:165], v[150:151], off offset:3072
	s_nop 0
	global_load_dwordx2 v[150:151], v[150:151], off offset:3584
.LrpN2_np:
	v_lshlrev_b32_e32 v96, 16, v82
	v_and_b32_e32 v97, 0xffff0000, v82
	v_lshlrev_b32_e32 v82, 16, v83
	v_and_b32_e32 v83, 0xffff0000, v83
	v_lshlrev_b32_e32 v99, 16, v85
	v_lshlrev_b32_e32 v98, 16, v84
	v_and_b32_e32 v85, 0xffff0000, v85
	v_and_b32_e32 v84, 0xffff0000, v84
	v_lshlrev_b32_e32 v103, 16, v88
	v_and_b32_e32 v105, 0xffff0000, v88
	v_and_b32_e32 v111, 0xffff0000, v94
	v_mul_f32_e32 v102, v83, v83
	v_mul_f32_e32 v104, v97, v97
	v_lshlrev_b32_e32 v100, 16, v86
	v_and_b32_e32 v101, 0xffff0000, v86
	v_lshlrev_b32_e32 v86, 16, v87
	v_and_b32_e32 v87, 0xffff0000, v87
	v_lshlrev_b32_e32 v110, 16, v94
	v_pk_mul_f32 v[116:117], v[84:85], v[84:85]
	v_mov_b32_e32 v119, v103
	v_mul_f32_e32 v118, v111, v111
	v_pk_fma_f32 v[126:127], v[82:83], v[82:83], v[102:103] op_sel_hi:[1,1,0]
	v_pk_fma_f32 v[128:129], v[96:97], v[96:97], v[104:105] op_sel_hi:[1,1,0]
	v_lshlrev_b32_e32 v88, 16, v89
	v_and_b32_e32 v89, 0xffff0000, v89
	v_lshlrev_b32_e32 v113, 16, v80
	v_and_b32_e32 v115, 0xffff0000, v80
	v_mul_f32_e32 v112, v101, v101
	v_mul_f32_e32 v114, v87, v87
	v_pk_fma_f32 v[116:117], v[98:99], v[98:99], v[116:117]
	v_pk_fma_f32 v[134:135], v[110:111], v[110:111], v[118:119] op_sel_hi:[1,1,0]
	v_mov_b32_e32 v102, v128
	v_mov_b32_e32 v118, v126
	v_mul_f32_e32 v79, v105, v105
	v_mul_f32_e32 v138, v88, v88
	v_mul_f32_e32 v139, v89, v89
	s_waitcnt lgkmcnt(0)
	v_pk_fma_f32 v[130:131], v[100:101], v[100:101], v[112:113] op_sel_hi:[1,1,0]
	v_pk_fma_f32 v[132:133], v[86:87], v[86:87], v[114:115] op_sel_hi:[1,1,0]
	v_pk_add_f32 v[126:127], v[128:129], v[126:127]
	v_pk_add_f32 v[116:117], v[116:117], v[116:117] op_sel:[0,1] op_sel_hi:[1,0]
	v_pk_mul_f32 v[118:119], v[102:103], v[118:119]
	v_lshlrev_b32_e32 v107, 16, v91
	v_lshlrev_b32_e32 v106, 16, v90
	v_and_b32_e32 v91, 0xffff0000, v91
	v_and_b32_e32 v90, 0xffff0000, v90
	v_mov_b32_e32 v131, v138
	v_mov_b32_e32 v133, v139
	v_mov_b32_e32 v117, v79
	v_mov_b32_e32 v127, v119
	v_pk_mul_f32 v[120:121], v[90:91], v[90:91]
	v_pk_add_f32 v[128:129], v[130:131], v[132:133]
	v_pk_add_f32 v[116:117], v[126:127], v[116:117]
	v_lshlrev_b32_e32 v109, 16, v93
	v_lshlrev_b32_e32 v108, 16, v92
	v_and_b32_e32 v93, 0xffff0000, v93
	v_and_b32_e32 v92, 0xffff0000, v92
	v_lshlrev_b32_e32 v94, 16, v95
	v_and_b32_e32 v95, 0xffff0000, v95
	v_pk_fma_f32 v[120:121], v[106:107], v[106:107], v[120:121]
	v_pk_add_f32 v[116:117], v[116:117], v[128:129]
	v_pk_mul_f32 v[122:123], v[92:93], v[92:93]
	v_mov_b32_e32 v125, v113
	v_mul_f32_e32 v124, v95, v95
	v_pk_add_f32 v[120:121], v[120:121], v[120:121] op_sel:[0,1] op_sel_hi:[1,0]
	v_pk_add_f32 v[116:117], v[116:117], v[116:117] op_sel:[0,1] op_sel_hi:[1,0]
	v_lshlrev_b32_e32 v80, 16, v81
	v_and_b32_e32 v81, 0xffff0000, v81
	v_pk_fma_f32 v[122:123], v[108:109], v[108:109], v[122:123]
	v_pk_fma_f32 v[136:137], v[94:95], v[94:95], v[124:125] op_sel_hi:[1,1,0]
	v_mov_b32_e32 v124, v120
	v_mov_b32_e32 v112, v116
	v_mul_f32_e32 v140, v115, v115
	v_mul_f32_e32 v141, v80, v80
	v_mul_f32_e32 v142, v81, v81
	v_pk_add_f32 v[122:123], v[122:123], v[122:123] op_sel:[0,1] op_sel_hi:[1,0]
	v_pk_add_f32 v[116:117], v[116:117], v[120:121]
	v_pk_mul_f32 v[118:119], v[112:113], v[124:125]
	v_mov_b32_e32 v135, v141
	v_mov_b32_e32 v137, v142
	v_mov_b32_e32 v123, v140
	v_mov_b32_e32 v117, v119
	v_pk_add_f32 v[116:117], v[116:117], v[122:123]
	v_pk_add_f32 v[118:119], v[134:135], v[136:137]
	v_mov_b32_e32 v104, v103
	v_pk_add_f32 v[116:117], v[116:117], v[118:119]
	v_mov_b32_e32 v114, v113
	v_add_f32_e32 v79, v116, v117
	ds_bpermute_b32 v102, v1, v79
	v_mov_b32_e32 v116, v98
	v_mov_b32_e32 v117, v84
	v_mov_b32_e32 v84, v99
	s_waitcnt lgkmcnt(0)
	v_add_f32_e32 v79, v79, v102
	ds_bpermute_b32 v102, v70, v79
	s_waitcnt lgkmcnt(0)
	v_add_f32_e32 v79, v79, v102
	ds_bpermute_b32 v102, v71, v79
	s_waitcnt lgkmcnt(0)
	v_add_f32_e32 v79, v79, v102
	ds_bpermute_b32 v102, v72, v79
	s_waitcnt lgkmcnt(0)
	v_add_f32_e32 v79, v79, v102
	ds_bpermute_b32 v102, v73, v79
	s_waitcnt lgkmcnt(0)
	v_add_f32_e32 v79, v79, v102
	ds_bpermute_b32 v102, v74, v79
	s_waitcnt lgkmcnt(0)
	v_add_f32_e32 v79, v79, v102
	v_fmamk_f32 v79, v79, 0x3a000000, v75
	v_mul_f32_e32 v98, 0x4f800000, v79
	v_cmp_gt_f32_e32 vcc, s5, v79
	s_nop 1
	v_cndmask_b32_e32 v79, v79, v98, vcc
	v_sqrt_f32_e32 v98, v79
	s_nop 0
	v_add_u32_e32 v99, -1, v98
	v_add_u32_e32 v102, 1, v98
	v_fma_f32 v103, -v99, v98, v79
	v_fma_f32 v112, -v102, v98, v79
	v_cmp_ge_f32_e64 s[2:3], 0, v103
	s_nop 1
	v_cndmask_b32_e64 v98, v98, v99, s[2:3]
	v_cmp_lt_f32_e64 s[2:3], 0, v112
	s_nop 1
	v_cndmask_b32_e64 v98, v98, v102, s[2:3]
	v_mul_f32_e32 v99, 0x37800000, v98
	v_cndmask_b32_e32 v98, v98, v99, vcc
	v_cmp_class_f32_e32 vcc, v79, v76
	s_nop 1
	v_cndmask_b32_e32 v79, v98, v79, vcc
	v_div_scale_f32 v99, s[2:3], v79, v79, 1.0
	v_rcp_f32_e32 v102, v99
	v_mov_b32_e32 v98, v106
	v_div_scale_f32 v103, vcc, 1.0, v79, 1.0
	v_fma_f32 v106, -v99, v102, 1.0
	v_fmac_f32_e32 v102, v106, v102
	v_mul_f32_e32 v106, v103, v102
	v_fma_f32 v112, -v99, v106, v103
	v_fmac_f32_e32 v106, v112, v102
	v_fma_f32 v99, -v99, v106, v103
	v_div_fmas_f32 v99, v99, v102, v106
	v_div_fixup_f32 v102, v99, v79, 1.0
	v_pk_mul_f32 v[96:97], v[102:103], v[96:97] op_sel_hi:[0,1]
	v_pk_mul_f32 v[82:83], v[102:103], v[82:83] op_sel_hi:[0,1]
	v_pk_mul_f32 v[116:117], v[102:103], v[116:117] op_sel_hi:[0,1]
	v_pk_mul_f32 v[84:85], v[102:103], v[84:85] op_sel_hi:[0,1]
	v_pk_fma_f32 v[82:83], v[34:35], v[82:83], v[4:5]
	v_pk_fma_f32 v[96:97], v[36:37], v[96:97], v[2:3]
	v_mov_b32_e32 v99, v90
	v_mov_b32_e32 v90, v107
	v_mov_b32_e32 v106, v108
	v_mov_b32_e32 v107, v92
	v_mov_b32_e32 v92, v109
	v_pk_mul_f32 v[108:109], v[102:103], v[110:111] op_sel_hi:[0,1]
	v_pk_mul_f32 v[110:111], v[114:115], v[102:103] op_sel_hi:[1,0]
	v_pk_mul_f32 v[100:101], v[102:103], v[100:101] op_sel_hi:[0,1]
	v_pk_mul_f32 v[86:87], v[102:103], v[86:87] op_sel_hi:[0,1]
	v_pk_mul_f32 v[104:105], v[104:105], v[102:103] op_sel_hi:[1,0]
	v_pk_mul_f32 v[88:89], v[88:89], v[102:103] op_sel_hi:[1,0]
	v_pk_fma_f32 v[84:85], v[38:39], v[84:85], v[8:9]
	v_pk_fma_f32 v[116:117], v[40:41], v[116:117], v[6:7]
	v_pk_mul_f32 v[98:99], v[102:103], v[98:99] op_sel_hi:[0,1]
	v_pk_mul_f32 v[90:91], v[102:103], v[90:91] op_sel_hi:[0,1]
	v_pk_mul_f32 v[106:107], v[102:103], v[106:107] op_sel_hi:[0,1]
	v_pk_mul_f32 v[92:93], v[102:103], v[92:93] op_sel_hi:[0,1]
	v_pk_mul_f32 v[94:95], v[102:103], v[94:95] op_sel_hi:[0,1]
	v_pk_mul_f32 v[80:81], v[80:81], v[102:103] op_sel_hi:[1,0]
	v_pk_fma_f32 v[102:103], v[64:65], v[110:111], v[30:31]
	v_max_f32_e64 v79, |v96|, |v97|
	v_max_f32_e64 v110, |v82|, |v83|
	v_pk_fma_f32 v[86:87], v[42:43], v[86:87], v[12:13]
	v_pk_fma_f32 v[100:101], v[44:45], v[100:101], v[10:11]
	v_max3_f32 v79, v79, 0, v110
	v_max_f32_e64 v110, |v116|, |v117|
	v_max_f32_e64 v111, |v84|, |v85|
	v_pk_fma_f32 v[88:89], v[46:47], v[88:89], v[16:17]
	v_pk_fma_f32 v[104:105], v[48:49], v[104:105], v[14:15]
	v_max3_f32 v79, v79, v110, v111
	v_max_f32_e64 v110, |v100|, |v101|
	v_max_f32_e64 v111, |v86|, |v87|
	v_pk_fma_f32 v[90:91], v[50:51], v[90:91], v[20:21]
	v_pk_fma_f32 v[98:99], v[52:53], v[98:99], v[18:19]
	v_max3_f32 v79, v79, v110, v111
	v_max_f32_e64 v110, |v104|, |v105|
	v_max_f32_e64 v111, |v88|, |v89|
	v_pk_fma_f32 v[92:93], v[54:55], v[92:93], v[24:25]
	v_pk_fma_f32 v[106:107], v[56:57], v[106:107], v[22:23]
	v_max3_f32 v79, v79, v110, v111
	v_max_f32_e64 v110, |v98|, |v99|
	v_max_f32_e64 v111, |v90|, |v91|
	v_pk_fma_f32 v[94:95], v[58:59], v[94:95], v[28:29]
	v_pk_fma_f32 v[108:109], v[60:61], v[108:109], v[26:27]
	v_max3_f32 v79, v79, v110, v111
	v_max_f32_e64 v110, |v106|, |v107|
	v_max_f32_e64 v111, |v92|, |v93|
	v_pk_fma_f32 v[80:81], v[62:63], v[80:81], v[32:33]
	v_max3_f32 v79, v79, v110, v111
	v_max_f32_e64 v110, |v108|, |v109|
	v_max_f32_e64 v111, |v94|, |v95|
	v_max3_f32 v79, v79, v110, v111
	v_max_f32_e64 v110, |v102|, |v103|
	v_max_f32_e64 v111, |v80|, |v81|
	v_max3_f32 v79, v79, v110, v111
	ds_bpermute_b32 v110, v1, v79
	s_waitcnt lgkmcnt(0)
	v_max_f32_e32 v110, v110, v110
	v_max_f32_e32 v79, v79, v110
	ds_bpermute_b32 v110, v70, v79
	s_waitcnt lgkmcnt(0)
	v_max_f32_e32 v110, v110, v110
	v_max_f32_e32 v79, v79, v110
	ds_bpermute_b32 v110, v71, v79
	s_waitcnt lgkmcnt(0)
	v_max_f32_e32 v110, v110, v110
	v_max_f32_e32 v79, v79, v110
	ds_bpermute_b32 v110, v72, v79
	s_waitcnt lgkmcnt(0)
	v_max_f32_e32 v110, v110, v110
	v_max_f32_e32 v79, v79, v110
	ds_bpermute_b32 v110, v73, v79
	s_waitcnt lgkmcnt(0)
	v_max_f32_e32 v110, v110, v110
	v_max_f32_e32 v79, v79, v110
	ds_bpermute_b32 v110, v74, v79
	s_waitcnt lgkmcnt(0)
	v_max_f32_e32 v110, v110, v110
	v_max_f32_e32 v79, v79, v110
	v_div_scale_f32 v110, s[2:3], v79, v79, s17
	v_rcp_f32_e32 v111, v110
	s_nop 0
	v_fma_f32 v112, -v110, v111, 1.0
	v_fmac_f32_e32 v111, v112, v111
	v_div_scale_f32 v112, vcc, s17, v79, s17
	v_mul_f32_e32 v113, v112, v111
	v_fma_f32 v114, -v110, v113, v112
	v_fmac_f32_e32 v113, v114, v111
	v_fma_f32 v110, -v110, v113, v112
	v_div_fmas_f32 v110, v110, v111, v113
	v_div_fixup_f32 v110, v110, v79, s17
	v_cmp_lt_f32_e32 vcc, 0, v79
	s_nop 1
	v_cndmask_b32_e32 v112, 0, v110, vcc
	v_mul_f32_e32 v97, v97, v112
	v_mul_f32_e32 v96, v96, v112
	v_mul_f32_e32 v82, v82, v112
	v_mul_f32_e32 v83, v83, v112
	v_med3_f32 v97, v97, s18, v78
	v_med3_f32 v96, v96, s18, v78
	v_add_f32_e32 v97, 0x4b400000, v97
	v_med3_f32 v82, v82, s18, v78
	v_med3_f32 v83, v83, s18, v78
	v_add_f32_e32 v96, 0x4b400000, v96
	v_add_f32_sdwa v82, v82, s19 dst_sel:WORD_1 dst_unused:UNUSED_PAD src0_sel:DWORD src1_sel:DWORD
	v_add_f32_e32 v83, 0x4b400000, v83
	v_lshlrev_b32_e32 v97, 8, v97
	v_lshl_add_u64 v[110:111], s[94:95], 0, v[66:67]
	v_and_b32_e32 v97, 0xff00, v97
	v_and_b32_e32 v82, 0xff0000, v82
	v_perm_b32 v83, v83, v96, s20
	v_or3_b32 v96, v83, v97, v82
	v_add_co_u32_e32 v82, vcc, s21, v110
	v_mul_f32_e32 v97, v117, v112
	s_nop 0
	v_addc_co_u32_e32 v83, vcc, 0, v111, vcc
	global_store_dword v[82:83], v96, off
	v_mul_f32_e32 v96, v116, v112
	v_mul_f32_e32 v84, v84, v112
	v_mul_f32_e32 v85, v85, v112
	v_med3_f32 v97, v97, s18, v78
	v_med3_f32 v96, v96, s18, v78
	v_add_f32_e32 v97, 0x4b400000, v97
	v_med3_f32 v84, v84, s18, v78
	v_med3_f32 v85, v85, s18, v78
	v_add_f32_e32 v96, 0x4b400000, v96
	v_add_f32_sdwa v84, v84, s19 dst_sel:WORD_1 dst_unused:UNUSED_PAD src0_sel:DWORD src1_sel:DWORD
	v_add_f32_e32 v85, 0x4b400000, v85
	v_lshlrev_b32_e32 v97, 8, v97
	v_and_b32_e32 v97, 0xff00, v97
	v_and_b32_e32 v84, 0xff0000, v84
	v_perm_b32 v85, v85, v96, s20
	v_or3_b32 v84, v85, v97, v84
	v_mul_f32_e32 v85, v101, v112
	global_store_dword v[82:83], v84, off offset:256
	v_mul_f32_e32 v84, v100, v112
	v_mul_f32_e32 v86, v86, v112
	v_mul_f32_e32 v87, v87, v112
	v_med3_f32 v85, v85, s18, v78
	v_med3_f32 v84, v84, s18, v78
	v_add_f32_e32 v85, 0x4b400000, v85
	v_med3_f32 v86, v86, s18, v78
	v_med3_f32 v87, v87, s18, v78
	v_add_f32_e32 v84, 0x4b400000, v84
	v_add_f32_sdwa v86, v86, s19 dst_sel:WORD_1 dst_unused:UNUSED_PAD src0_sel:DWORD src1_sel:DWORD
	v_add_f32_e32 v87, 0x4b400000, v87
	v_lshlrev_b32_e32 v85, 8, v85
	v_and_b32_e32 v85, 0xff00, v85
	v_and_b32_e32 v86, 0xff0000, v86
	v_perm_b32 v84, v87, v84, s20
	v_or3_b32 v84, v84, v85, v86
	v_mul_f32_e32 v85, v105, v112
	global_store_dword v[82:83], v84, off offset:512
	v_mul_f32_e32 v84, v104, v112
	v_mul_f32_e32 v86, v88, v112
	v_mul_f32_e32 v87, v89, v112
	v_med3_f32 v85, v85, s18, v78
	v_med3_f32 v84, v84, s18, v78
	v_add_f32_e32 v85, 0x4b400000, v85
	v_med3_f32 v86, v86, s18, v78
	v_med3_f32 v87, v87, s18, v78
	v_add_f32_e32 v84, 0x4b400000, v84
	v_add_f32_sdwa v86, v86, s19 dst_sel:WORD_1 dst_unused:UNUSED_PAD src0_sel:DWORD src1_sel:DWORD
	v_add_f32_e32 v87, 0x4b400000, v87
	v_lshlrev_b32_e32 v85, 8, v85
	v_and_b32_e32 v85, 0xff00, v85
	v_and_b32_e32 v86, 0xff0000, v86
	v_perm_b32 v84, v87, v84, s20
	v_or3_b32 v84, v84, v85, v86
	v_mul_f32_e32 v85, v99, v112
	global_store_dword v[82:83], v84, off offset:768
	v_mul_f32_e32 v84, v98, v112
	v_mul_f32_e32 v86, v90, v112
	v_mul_f32_e32 v87, v91, v112
	v_med3_f32 v85, v85, s18, v78
	v_med3_f32 v84, v84, s18, v78
	v_add_f32_e32 v85, 0x4b400000, v85
	v_med3_f32 v86, v86, s18, v78
	v_med3_f32 v87, v87, s18, v78
	v_add_f32_e32 v84, 0x4b400000, v84
	v_add_f32_sdwa v86, v86, s19 dst_sel:WORD_1 dst_unused:UNUSED_PAD src0_sel:DWORD src1_sel:DWORD
	v_add_f32_e32 v87, 0x4b400000, v87
	v_lshlrev_b32_e32 v85, 8, v85
	v_and_b32_e32 v85, 0xff00, v85
	v_and_b32_e32 v86, 0xff0000, v86
	v_perm_b32 v84, v87, v84, s20
	v_or3_b32 v84, v84, v85, v86
	v_mul_f32_e32 v85, v107, v112
	global_store_dword v[82:83], v84, off offset:1024
	v_mul_f32_e32 v84, v106, v112
	v_mul_f32_e32 v86, v92, v112
	v_mul_f32_e32 v87, v93, v112
	v_med3_f32 v85, v85, s18, v78
	v_med3_f32 v84, v84, s18, v78
	v_add_f32_e32 v85, 0x4b400000, v85
	v_med3_f32 v86, v86, s18, v78
	v_med3_f32 v87, v87, s18, v78
	v_add_f32_e32 v84, 0x4b400000, v84
	v_add_f32_sdwa v86, v86, s19 dst_sel:WORD_1 dst_unused:UNUSED_PAD src0_sel:DWORD src1_sel:DWORD
	v_add_f32_e32 v87, 0x4b400000, v87
	v_lshlrev_b32_e32 v85, 8, v85
	v_and_b32_e32 v85, 0xff00, v85
	v_and_b32_e32 v86, 0xff0000, v86
	v_perm_b32 v84, v87, v84, s20
	v_or3_b32 v84, v84, v85, v86
	v_mul_f32_e32 v85, v109, v112
	global_store_dword v[82:83], v84, off offset:1280
	v_mul_f32_e32 v84, v108, v112
	v_mul_f32_e32 v86, v94, v112
	v_mul_f32_e32 v87, v95, v112
	v_med3_f32 v85, v85, s18, v78
	v_med3_f32 v84, v84, s18, v78
	v_add_f32_e32 v85, 0x4b400000, v85
	v_med3_f32 v86, v86, s18, v78
	v_med3_f32 v87, v87, s18, v78
	v_add_f32_e32 v84, 0x4b400000, v84
	v_add_f32_sdwa v86, v86, s19 dst_sel:WORD_1 dst_unused:UNUSED_PAD src0_sel:DWORD src1_sel:DWORD
	v_add_f32_e32 v87, 0x4b400000, v87
	v_lshlrev_b32_e32 v85, 8, v85
	v_and_b32_e32 v85, 0xff00, v85
	v_and_b32_e32 v86, 0xff0000, v86
	v_perm_b32 v84, v87, v84, s20
	v_or3_b32 v84, v84, v85, v86
	v_mul_f32_e32 v85, v103, v112
	global_store_dword v[82:83], v84, off offset:1536
	v_mul_f32_e32 v84, v102, v112
	v_mul_f32_e32 v80, v80, v112
	v_mul_f32_e32 v81, v81, v112
	v_med3_f32 v85, v85, s18, v78
	v_med3_f32 v84, v84, s18, v78
	v_add_f32_e32 v85, 0x4b400000, v85
	v_med3_f32 v80, v80, s18, v78
	v_med3_f32 v81, v81, s18, v78
	v_add_f32_e32 v84, 0x4b400000, v84
	v_add_f32_sdwa v80, v80, s19 dst_sel:WORD_1 dst_unused:UNUSED_PAD src0_sel:DWORD src1_sel:DWORD
	v_add_f32_e32 v81, 0x4b400000, v81
	v_lshlrev_b32_e32 v85, 8, v85
	v_and_b32_e32 v85, 0xff00, v85
	v_and_b32_e32 v80, 0xff0000, v80
	v_perm_b32 v81, v81, v84, s20
	v_or3_b32 v80, v81, v85, v80
	global_store_dword v[82:83], v80, off offset:1792
	s_and_saveexec_b64 s[2:3], s[0:1]
	s_cbranch_execz .LBB0_1433
	s_add_u32 s22, s94, s11
	s_addc_u32 s23, s95, s16
	v_mul_f32_e32 v79, 0x3c010204, v79
	global_store_dword v77, v79, s[22:23]
	s_branch .LBB0_1433

.LBB0_1825:
	s_cmp_gt_i32 s96, 11
	s_cselect_b64 s[0:1], -1, 0
	s_cmp_lt_i32 s97, 12
	s_cselect_b64 s[2:3], -1, 0
	s_or_b64 s[0:1], s[0:1], s[2:3]
	s_and_b64 vcc, exec, s[0:1]
	s_cbranch_vccnz .LBB0_1881
	v_readfirstlane_b32 s1, v0
	s_lshl_b32 s0, s8, 3
	s_lshr_b32 s2, s1, 6
	s_add_i32 s0, s2, s0
	s_ashr_i32 s10, s0, 1
	s_cmpk_gt_i32 s10, 0xfff
	s_cbranch_scc1 .LBB0_1831
	v_readlane_b32 s16, v254, 2
	v_readlane_b32 s17, v254, 3
	v_readlane_b32 s18, v254, 4
	v_readlane_b32 s19, v254, 5
	v_readlane_b32 s20, v254, 6
	v_readlane_b32 s21, v254, 7
	v_readlane_b32 s22, v254, 8
	v_readlane_b32 s23, v254, 9
	v_readlane_b32 s24, v254, 10
	v_readlane_b32 s25, v254, 11
	v_readlane_b32 s26, v254, 12
	v_readlane_b32 s27, v254, 13
	v_readlane_b32 s28, v254, 14
	v_readlane_b32 s29, v254, 15
	v_readlane_b32 s30, v254, 16
	v_readlane_b32 s31, v254, 17
	s_mov_b64 s[16:17], s[24:25]
	s_add_u32 s0, s16, 0x2000
	s_addc_u32 s1, s17, 0
	s_and_b32 s5, s2, 1
	s_lshl_b32 s4, s9, 2
	s_mul_i32 s2, s5, 0xc000
	s_add_u32 s6, s94, s2
	s_addc_u32 s7, s95, 0
	v_and_b32_e32 v114, 63, v0
	s_add_u32 s2, s6, 0x11a000
	v_lshlrev_b32_e32 v1, 4, v114
	s_addc_u32 s3, s7, 0
	s_waitcnt vmcnt(15)
	v_mov_b32_e32 v2, 0x1c00
	global_load_dwordx4 v[34:37], v1, s[2:3]
	global_load_dwordx4 v[38:41], v1, s[2:3] offset:1024
	s_waitcnt vmcnt(13)
	v_or_b32_e32 v18, 0x1000, v1
	s_waitcnt vmcnt(12)
	v_or_b32_e32 v22, 0x1400, v1
	s_waitcnt vmcnt(11)
	v_or_b32_e32 v26, 0x1800, v1
	s_waitcnt vmcnt(10)
	v_lshl_or_b32 v30, v0, 4, v2
	v_or_b32_e32 v2, 0x400, v1
	global_load_dwordx4 v[42:45], v1, s[2:3] offset:2048
	global_load_dwordx4 v[46:49], v18, s[2:3]
	global_load_dwordx4 v[50:53], v22, s[2:3]
	global_load_dwordx4 v[54:57], v26, s[2:3]
	global_load_dwordx4 v[58:61], v30, s[2:3]
	global_load_dwordx4 v[62:65], v1, s[0:1]
	global_load_dwordx4 v[66:69], v2, s[0:1]
	v_or_b32_e32 v2, 0x800, v1
	v_mbcnt_lo_u32_b32 v6, -1, 0
	global_load_dwordx4 v[72:75], v2, s[0:1]
	global_load_dwordx4 v[76:79], v18, s[0:1]
	global_load_dwordx4 v[80:83], v22, s[0:1]
	global_load_dwordx4 v[84:87], v26, s[0:1]
	global_load_dwordx4 v[88:91], v30, s[0:1]
	global_load_dwordx4 v[92:95], v1, s[2:3] offset:3072
	s_add_u32 s2, s6, 0x118000
	v_mbcnt_hi_u32_b32 v115, -1, v6
	v_or_b32_e32 v2, 0xc00, v1
	s_addc_u32 s3, s7, 0
	v_and_b32_e32 v6, 64, v115
	global_load_dwordx4 v[96:99], v2, s[0:1]
	v_add_u32_e32 v116, 64, v6
	global_load_dwordx4 v[2:5], v1, s[2:3]
	global_load_dwordx4 v[6:9], v1, s[2:3] offset:1024
	global_load_dwordx4 v[10:13], v1, s[2:3] offset:2048
	global_load_dwordx4 v[14:17], v1, s[2:3] offset:3072
	s_nop 0
	global_load_dwordx4 v[18:21], v18, s[2:3]
	s_nop 0
	global_load_dwordx4 v[22:25], v22, s[2:3]
	s_nop 0
	global_load_dwordx4 v[26:29], v26, s[2:3]
	s_nop 0
	global_load_dwordx4 v[30:33], v30, s[2:3]
	v_xor_b32_e32 v70, 1, v115
	v_xor_b32_e32 v71, 2, v115
	v_cmp_lt_i32_e32 vcc, v70, v116
	s_lshl_b32 s2, s5, 12
	s_add_i32 s2, s10, s2
	v_cndmask_b32_e32 v1, v115, v70, vcc
	v_cmp_lt_i32_e32 vcc, v71, v116
	s_ashr_i32 s3, s2, 31
	s_lshl_b64 s[6:7], s[2:3], 2
	v_cndmask_b32_e32 v70, v115, v71, vcc
	s_mov_b64 s[18:19], s[26:27]
	s_add_u32 s11, s6, 0x2c8000
	s_mov_b64 s[20:21], s[28:29]
	s_mov_b64 s[22:23], s[30:31]
	s_addc_u32 s16, s7, 0
	s_ashr_i32 s5, s4, 31
	s_lshl_b64 s[18:19], s[2:3], 11
	s_lshl_b64 s[2:3], s[2:3], 12
	v_cmp_eq_u32_e64 s[0:1], 0, v114
	v_lshlrev_b32_e32 v1, 2, v1
	v_lshlrev_b32_e32 v70, 2, v70
	s_lshl_b64 s[6:7], s[4:5], 2
	s_lshl_b64 s[20:21], s[4:5], 11
	s_lshl_b64 s[34:35], s[4:5], 12
	s_mov_b32 s5, 0xf800000
	s_mov_b32 s17, 0x42fe0000
	s_mov_b32 s22, 0x40c0c00
	s_mov_b32 s23, 0x36200000
	s_waitcnt vmcnt(23)
	v_pk_add_f32 v[36:37], v[36:37], 1.0 op_sel_hi:[1,0]
	s_waitcnt vmcnt(22)
	v_pk_add_f32 v[40:41], v[40:41], 1.0 op_sel_hi:[1,0]
	v_pk_add_f32 v[102:103], v[38:39], 1.0 op_sel_hi:[1,0]
	v_pk_add_f32 v[100:101], v[34:35], 1.0 op_sel_hi:[1,0]
	s_waitcnt vmcnt(21)
	v_pk_add_f32 v[44:45], v[44:45], 1.0 op_sel_hi:[1,0]
	v_pk_add_f32 v[104:105], v[42:43], 1.0 op_sel_hi:[1,0]
	s_waitcnt vmcnt(20)
	v_pk_add_f32 v[48:49], v[48:49], 1.0 op_sel_hi:[1,0]
	s_waitcnt vmcnt(14)
	v_pk_mul_f32 v[42:43], v[74:75], v[44:45]
	v_pk_mul_f32 v[44:45], v[72:73], v[104:105]
	v_pk_mul_f32 v[38:39], v[68:69], v[40:41]
	v_pk_mul_f32 v[40:41], v[66:67], v[102:103]
	v_xor_b32_e32 v66, 4, v115
	v_cmp_lt_i32_e32 vcc, v66, v116
	v_pk_add_f32 v[106:107], v[46:47], 1.0 op_sel_hi:[1,0]
	v_pk_add_f32 v[52:53], v[52:53], 1.0 op_sel_hi:[1,0]
	v_cndmask_b32_e32 v66, v115, v66, vcc
	v_lshlrev_b32_e32 v71, 2, v66
	v_xor_b32_e32 v66, 8, v115
	v_cmp_lt_i32_e32 vcc, v66, v116
	v_pk_add_f32 v[108:109], v[50:51], 1.0 op_sel_hi:[1,0]
	v_pk_add_f32 v[56:57], v[56:57], 1.0 op_sel_hi:[1,0]
	v_cndmask_b32_e32 v66, v115, v66, vcc
	v_lshlrev_b32_e32 v72, 2, v66
	v_xor_b32_e32 v66, 16, v115
	v_cmp_lt_i32_e32 vcc, v66, v116
	v_pk_add_f32 v[110:111], v[54:55], 1.0 op_sel_hi:[1,0]
	v_pk_add_f32 v[60:61], v[60:61], 1.0 op_sel_hi:[1,0]
	v_cndmask_b32_e32 v66, v115, v66, vcc
	v_lshlrev_b32_e32 v73, 2, v66
	v_xor_b32_e32 v66, 32, v115
	v_cmp_lt_i32_e32 vcc, v66, v116
	v_pk_add_f32 v[112:113], v[58:59], 1.0 op_sel_hi:[1,0]
	v_pk_mul_f32 v[34:35], v[64:65], v[36:37]
	v_pk_mul_f32 v[36:37], v[62:63], v[100:101]
	s_waitcnt vmcnt(9)
	v_pk_add_f32 v[62:63], v[94:95], 1.0 op_sel_hi:[1,0]
	v_pk_add_f32 v[64:65], v[92:93], 1.0 op_sel_hi:[1,0]
	v_cndmask_b32_e32 v66, v115, v66, vcc
	v_pk_mul_f32 v[46:47], v[78:79], v[48:49]
	v_pk_mul_f32 v[48:49], v[76:77], v[106:107]
	v_pk_mul_f32 v[50:51], v[82:83], v[52:53]
	v_pk_mul_f32 v[52:53], v[80:81], v[108:109]
	v_pk_mul_f32 v[54:55], v[86:87], v[56:57]
	v_pk_mul_f32 v[56:57], v[84:85], v[110:111]
	v_pk_mul_f32 v[58:59], v[90:91], v[60:61]
	v_pk_mul_f32 v[60:61], v[88:89], v[112:113]
	s_waitcnt vmcnt(8)
	v_pk_mul_f32 v[62:63], v[98:99], v[62:63]
	v_pk_mul_f32 v[64:65], v[96:97], v[64:65]
	v_lshlrev_b32_e32 v74, 2, v66
	v_lshl_or_b32 v66, v114, 2, s18
	v_mov_b32_e32 v67, s19
	v_lshl_or_b32 v68, v114, 3, s2
	v_mov_b32_e32 v69, s3
	v_mov_b32_e32 v75, 0x358637bd
	v_mov_b32_e32 v76, 0x260
	s_mov_b32 s18, 0xc2fe0000
	s_mov_b32 s19, 0x4b400000
	v_mov_b32_e32 v77, 0
	v_mov_b32_e32 v78, 0x42fe0000
	v_lshl_add_u64 v[150:151], s[94:95], 0, v[68:69]
	v_add_co_u32_e32 v150, vcc, 0x4c200000, v150
	s_nop 1
	v_addc_co_u32_e32 v151, vcc, 0, v151, vcc
	global_load_dwordx2 v[152:153], v[150:151], off
	global_load_dwordx2 v[154:155], v[150:151], off offset:512
	global_load_dwordx2 v[156:157], v[150:151], off offset:1024
	global_load_dwordx2 v[158:159], v[150:151], off offset:1536
	global_load_dwordx2 v[160:161], v[150:151], off offset:2048
	global_load_dwordx2 v[162:163], v[150:151], off offset:2560
	global_load_dwordx2 v[164:165], v[150:151], off offset:3072
	s_nop 0
	global_load_dwordx2 v[150:151], v[150:151], off offset:3584
	s_waitcnt vmcnt(0)
	s_branch .LrpN3_in

.LrpN3_in:
	v_mov_b32_e32 v80, v150
	v_mov_b32_e32 v81, v151
	v_mov_b32_e32 v82, v152
	v_mov_b32_e32 v83, v153
	v_mov_b32_e32 v84, v154
	v_mov_b32_e32 v85, v155
	v_mov_b32_e32 v86, v156
	v_mov_b32_e32 v87, v157
	v_mov_b32_e32 v88, v158
	v_mov_b32_e32 v89, v159
	v_mov_b32_e32 v90, v160
	v_mov_b32_e32 v91, v161
	v_mov_b32_e32 v92, v162
	v_mov_b32_e32 v93, v163
	v_mov_b32_e32 v94, v164
	v_mov_b32_e32 v95, v165
	s_add_i32 s24, s10, s4
	s_cmpk_lt_i32 s24, 0x1000
	s_cbranch_scc0 .LrpN3_np
	v_lshl_add_u64 v[146:147], v[68:69], 0, s[34:35]
	v_lshl_add_u64 v[150:151], s[94:95], 0, v[146:147]
	v_add_co_u32_e32 v150, vcc, 0x4c200000, v150
	s_nop 1
	v_addc_co_u32_e32 v151, vcc, 0, v151, vcc
	global_load_dwordx2 v[152:153], v[150:151], off
	global_load_dwordx2 v[154:155], v[150:151], off offset:512
	global_load_dwordx2 v[156:157], v[150:151], off offset:1024
	global_load_dwordx2 v[158:159], v[150:151], off offset:1536
	global_load_dwordx2 v[160:161], v[150:151], off offset:2048
	global_load_dwordx2 v[162:163], v[150:151], off offset:2560
	global_load_dwordx2 v[164:165], v[150:151], off offset:3072
	s_nop 0
	global_load_dwordx2 v[150:151], v[150:151], off offset:3584
.LrpN3_np:
	v_lshlrev_b32_e32 v96, 16, v82
	v_and_b32_e32 v97, 0xffff0000, v82
	v_lshlrev_b32_e32 v82, 16, v83
	v_and_b32_e32 v83, 0xffff0000, v83
	v_lshlrev_b32_e32 v99, 16, v85
	v_lshlrev_b32_e32 v98, 16, v84
	v_and_b32_e32 v85, 0xffff0000, v85
	v_and_b32_e32 v84, 0xffff0000, v84
	v_lshlrev_b32_e32 v103, 16, v88
	v_and_b32_e32 v105, 0xffff0000, v88
	v_and_b32_e32 v111, 0xffff0000, v94
	v_mul_f32_e32 v102, v83, v83
	v_mul_f32_e32 v104, v97, v97
	v_lshlrev_b32_e32 v100, 16, v86
	v_and_b32_e32 v101, 0xffff0000, v86
	v_lshlrev_b32_e32 v86, 16, v87
	v_and_b32_e32 v87, 0xffff0000, v87
	v_lshlrev_b32_e32 v110, 16, v94
	v_pk_mul_f32 v[116:117], v[84:85], v[84:85]
	v_mov_b32_e32 v119, v103
	v_mul_f32_e32 v118, v111, v111
	v_pk_fma_f32 v[126:127], v[82:83], v[82:83], v[102:103] op_sel_hi:[1,1,0]
	v_pk_fma_f32 v[128:129], v[96:97], v[96:97], v[104:105] op_sel_hi:[1,1,0]
	v_lshlrev_b32_e32 v88, 16, v89
	v_and_b32_e32 v89, 0xffff0000, v89
	v_lshlrev_b32_e32 v113, 16, v80
	v_and_b32_e32 v115, 0xffff0000, v80
	v_mul_f32_e32 v112, v101, v101
	v_mul_f32_e32 v114, v87, v87
	v_pk_fma_f32 v[116:117], v[98:99], v[98:99], v[116:117]
	v_pk_fma_f32 v[134:135], v[110:111], v[110:111], v[118:119] op_sel_hi:[1,1,0]
	v_mov_b32_e32 v102, v128
	v_mov_b32_e32 v118, v126
	v_mul_f32_e32 v79, v105, v105
	v_mul_f32_e32 v138, v88, v88
	v_mul_f32_e32 v139, v89, v89
	s_waitcnt lgkmcnt(0)
	v_pk_fma_f32 v[130:131], v[100:101], v[100:101], v[112:113] op_sel_hi:[1,1,0]
	v_pk_fma_f32 v[132:133], v[86:87], v[86:87], v[114:115] op_sel_hi:[1,1,0]
	v_pk_add_f32 v[126:127], v[128:129], v[126:127]
	v_pk_add_f32 v[116:117], v[116:117], v[116:117] op_sel:[0,1] op_sel_hi:[1,0]
	v_pk_mul_f32 v[118:119], v[102:103], v[118:119]
	v_lshlrev_b32_e32 v107, 16, v91
	v_lshlrev_b32_e32 v106, 16, v90
	v_and_b32_e32 v91, 0xffff0000, v91
	v_and_b32_e32 v90, 0xffff0000, v90
	v_mov_b32_e32 v131, v138
	v_mov_b32_e32 v133, v139
	v_mov_b32_e32 v117, v79
	v_mov_b32_e32 v127, v119
	v_pk_mul_f32 v[120:121], v[90:91], v[90:91]
	v_pk_add_f32 v[128:129], v[130:131], v[132:133]
	v_pk_add_f32 v[116:117], v[126:127], v[116:117]
	v_lshlrev_b32_e32 v109, 16, v93
	v_lshlrev_b32_e32 v108, 16, v92
	v_and_b32_e32 v93, 0xffff0000, v93
	v_and_b32_e32 v92, 0xffff0000, v92
	v_lshlrev_b32_e32 v94, 16, v95
	v_and_b32_e32 v95, 0xffff0000, v95
	v_pk_fma_f32 v[120:121], v[106:107], v[106:107], v[120:121]
	v_pk_add_f32 v[116:117], v[116:117], v[128:129]
	v_pk_mul_f32 v[122:123], v[92:93], v[92:93]
	v_mov_b32_e32 v125, v113
	v_mul_f32_e32 v124, v95, v95
	v_pk_add_f32 v[120:121], v[120:121], v[120:121] op_sel:[0,1] op_sel_hi:[1,0]
	v_pk_add_f32 v[116:117], v[116:117], v[116:117] op_sel:[0,1] op_sel_hi:[1,0]
	v_lshlrev_b32_e32 v80, 16, v81
	v_and_b32_e32 v81, 0xffff0000, v81
	v_pk_fma_f32 v[122:123], v[108:109], v[108:109], v[122:123]
	v_pk_fma_f32 v[136:137], v[94:95], v[94:95], v[124:125] op_sel_hi:[1,1,0]
	v_mov_b32_e32 v124, v120
	v_mov_b32_e32 v112, v116
	v_mul_f32_e32 v140, v115, v115
	v_mul_f32_e32 v141, v80, v80
	v_mul_f32_e32 v142, v81, v81
	v_pk_add_f32 v[122:123], v[122:123], v[122:123] op_sel:[0,1] op_sel_hi:[1,0]
	v_pk_add_f32 v[116:117], v[116:117], v[120:121]
	v_pk_mul_f32 v[118:119], v[112:113], v[124:125]
	v_mov_b32_e32 v135, v141
	v_mov_b32_e32 v137, v142
	v_mov_b32_e32 v123, v140
	v_mov_b32_e32 v117, v119
	v_pk_add_f32 v[116:117], v[116:117], v[122:123]
	v_pk_add_f32 v[118:119], v[134:135], v[136:137]
	v_mov_b32_e32 v104, v103
	v_pk_add_f32 v[116:117], v[116:117], v[118:119]
	v_mov_b32_e32 v114, v113
	v_add_f32_e32 v79, v116, v117
	ds_bpermute_b32 v102, v1, v79
	v_mov_b32_e32 v116, v98
	v_mov_b32_e32 v117, v84
	v_mov_b32_e32 v84, v99
	s_waitcnt lgkmcnt(0)
	v_add_f32_e32 v79, v79, v102
	ds_bpermute_b32 v102, v70, v79
	s_waitcnt lgkmcnt(0)
	v_add_f32_e32 v79, v79, v102
	ds_bpermute_b32 v102, v71, v79
	s_waitcnt lgkmcnt(0)
	v_add_f32_e32 v79, v79, v102
	ds_bpermute_b32 v102, v72, v79
	s_waitcnt lgkmcnt(0)
	v_add_f32_e32 v79, v79, v102
	ds_bpermute_b32 v102, v73, v79
	s_waitcnt lgkmcnt(0)
	v_add_f32_e32 v79, v79, v102
	ds_bpermute_b32 v102, v74, v79
	s_waitcnt lgkmcnt(0)
	v_add_f32_e32 v79, v79, v102
	v_fmamk_f32 v79, v79, 0x3a000000, v75
	v_mul_f32_e32 v98, 0x4f800000, v79
	v_cmp_gt_f32_e32 vcc, s5, v79
	s_nop 1
	v_cndmask_b32_e32 v79, v79, v98, vcc
	v_sqrt_f32_e32 v98, v79
	s_nop 0
	v_add_u32_e32 v99, -1, v98
	v_add_u32_e32 v102, 1, v98
	v_fma_f32 v103, -v99, v98, v79
	v_fma_f32 v112, -v102, v98, v79
	v_cmp_ge_f32_e64 s[2:3], 0, v103
	s_nop 1
	v_cndmask_b32_e64 v98, v98, v99, s[2:3]
	v_cmp_lt_f32_e64 s[2:3], 0, v112
	s_nop 1
	v_cndmask_b32_e64 v98, v98, v102, s[2:3]
	v_mul_f32_e32 v99, 0x37800000, v98
	v_cndmask_b32_e32 v98, v98, v99, vcc
	v_cmp_class_f32_e32 vcc, v79, v76
	s_nop 1
	v_cndmask_b32_e32 v79, v98, v79, vcc
	v_div_scale_f32 v99, s[2:3], v79, v79, 1.0
	v_rcp_f32_e32 v102, v99
	v_mov_b32_e32 v98, v106
	v_div_scale_f32 v103, vcc, 1.0, v79, 1.0
	v_fma_f32 v106, -v99, v102, 1.0
	v_fmac_f32_e32 v102, v106, v102
	v_mul_f32_e32 v106, v103, v102
	v_fma_f32 v112, -v99, v106, v103
	v_fmac_f32_e32 v106, v112, v102
	v_fma_f32 v99, -v99, v106, v103
	v_div_fmas_f32 v99, v99, v102, v106
	v_div_fixup_f32 v102, v99, v79, 1.0
	v_pk_mul_f32 v[96:97], v[102:103], v[96:97] op_sel_hi:[0,1]
	v_pk_mul_f32 v[82:83], v[102:103], v[82:83] op_sel_hi:[0,1]
	v_pk_mul_f32 v[116:117], v[102:103], v[116:117] op_sel_hi:[0,1]
	v_pk_mul_f32 v[84:85], v[102:103], v[84:85] op_sel_hi:[0,1]
	v_pk_fma_f32 v[82:83], v[34:35], v[82:83], v[4:5]
	v_pk_fma_f32 v[96:97], v[36:37], v[96:97], v[2:3]
	v_mov_b32_e32 v99, v90
	v_mov_b32_e32 v90, v107
	v_mov_b32_e32 v106, v108
	v_mov_b32_e32 v107, v92
	v_mov_b32_e32 v92, v109
	v_pk_mul_f32 v[108:109], v[102:103], v[110:111] op_sel_hi:[0,1]
	v_pk_mul_f32 v[110:111], v[114:115], v[102:103] op_sel_hi:[1,0]
	v_pk_mul_f32 v[100:101], v[102:103], v[100:101] op_sel_hi:[0,1]
	v_pk_mul_f32 v[86:87], v[102:103], v[86:87] op_sel_hi:[0,1]
	v_pk_mul_f32 v[104:105], v[104:105], v[102:103] op_sel_hi:[1,0]
	v_pk_mul_f32 v[88:89], v[88:89], v[102:103] op_sel_hi:[1,0]
	v_pk_fma_f32 v[84:85], v[38:39], v[84:85], v[8:9]
	v_pk_fma_f32 v[116:117], v[40:41], v[116:117], v[6:7]
	v_pk_mul_f32 v[98:99], v[102:103], v[98:99] op_sel_hi:[0,1]
	v_pk_mul_f32 v[90:91], v[102:103], v[90:91] op_sel_hi:[0,1]
	v_pk_mul_f32 v[106:107], v[102:103], v[106:107] op_sel_hi:[0,1]
	v_pk_mul_f32 v[92:93], v[102:103], v[92:93] op_sel_hi:[0,1]
	v_pk_mul_f32 v[94:95], v[102:103], v[94:95] op_sel_hi:[0,1]
	v_pk_mul_f32 v[80:81], v[80:81], v[102:103] op_sel_hi:[1,0]
	v_pk_fma_f32 v[102:103], v[60:61], v[110:111], v[30:31]
	v_max_f32_e64 v79, |v96|, |v97|
	v_max_f32_e64 v110, |v82|, |v83|
	v_pk_fma_f32 v[86:87], v[42:43], v[86:87], v[12:13]
	v_pk_fma_f32 v[100:101], v[44:45], v[100:101], v[10:11]
	v_max3_f32 v79, v79, 0, v110
	v_max_f32_e64 v110, |v116|, |v117|
	v_max_f32_e64 v111, |v84|, |v85|
	v_pk_fma_f32 v[88:89], v[62:63], v[88:89], v[16:17]
	v_pk_fma_f32 v[104:105], v[64:65], v[104:105], v[14:15]
	v_max3_f32 v79, v79, v110, v111
	v_max_f32_e64 v110, |v100|, |v101|
	v_max_f32_e64 v111, |v86|, |v87|
	v_pk_fma_f32 v[90:91], v[46:47], v[90:91], v[20:21]
	v_pk_fma_f32 v[98:99], v[48:49], v[98:99], v[18:19]
	v_max3_f32 v79, v79, v110, v111
	v_max_f32_e64 v110, |v104|, |v105|
	v_max_f32_e64 v111, |v88|, |v89|
	v_pk_fma_f32 v[92:93], v[50:51], v[92:93], v[24:25]
	v_pk_fma_f32 v[106:107], v[52:53], v[106:107], v[22:23]
	v_max3_f32 v79, v79, v110, v111
	v_max_f32_e64 v110, |v98|, |v99|
	v_max_f32_e64 v111, |v90|, |v91|
	v_pk_fma_f32 v[94:95], v[54:55], v[94:95], v[28:29]
	v_pk_fma_f32 v[108:109], v[56:57], v[108:109], v[26:27]
	v_max3_f32 v79, v79, v110, v111
	v_max_f32_e64 v110, |v106|, |v107|
	v_max_f32_e64 v111, |v92|, |v93|
	v_pk_fma_f32 v[80:81], v[58:59], v[80:81], v[32:33]
	v_max3_f32 v79, v79, v110, v111
	v_max_f32_e64 v110, |v108|, |v109|
	v_max_f32_e64 v111, |v94|, |v95|
	v_max3_f32 v79, v79, v110, v111
	v_max_f32_e64 v110, |v102|, |v103|
	v_max_f32_e64 v111, |v80|, |v81|
	v_max3_f32 v79, v79, v110, v111
	ds_bpermute_b32 v110, v1, v79
	s_waitcnt lgkmcnt(0)
	v_max_f32_e32 v110, v110, v110
	v_max_f32_e32 v79, v79, v110
	ds_bpermute_b32 v110, v70, v79
	s_waitcnt lgkmcnt(0)
	v_max_f32_e32 v110, v110, v110
	v_max_f32_e32 v79, v79, v110
	ds_bpermute_b32 v110, v71, v79
	s_waitcnt lgkmcnt(0)
	v_max_f32_e32 v110, v110, v110
	v_max_f32_e32 v79, v79, v110
	ds_bpermute_b32 v110, v72, v79
	s_waitcnt lgkmcnt(0)
	v_max_f32_e32 v110, v110, v110
	v_max_f32_e32 v79, v79, v110
	ds_bpermute_b32 v110, v73, v79
	s_waitcnt lgkmcnt(0)
	v_max_f32_e32 v110, v110, v110
	v_max_f32_e32 v79, v79, v110
	ds_bpermute_b32 v110, v74, v79
	s_waitcnt lgkmcnt(0)
	v_max_f32_e32 v110, v110, v110
	v_max_f32_e32 v79, v79, v110
	v_div_scale_f32 v110, s[2:3], v79, v79, s17
	v_rcp_f32_e32 v111, v110
	s_nop 0
	v_fma_f32 v112, -v110, v111, 1.0
	v_fmac_f32_e32 v111, v112, v111
	v_div_scale_f32 v112, vcc, s17, v79, s17
	v_mul_f32_e32 v113, v112, v111
	v_fma_f32 v114, -v110, v113, v112
	v_fmac_f32_e32 v113, v114, v111
	v_fma_f32 v110, -v110, v113, v112
	v_div_fmas_f32 v110, v110, v111, v113
	v_div_fixup_f32 v110, v110, v79, s17
	v_cmp_lt_f32_e32 vcc, 0, v79
	s_nop 1
	v_cndmask_b32_e32 v112, 0, v110, vcc
	v_mul_f32_e32 v97, v97, v112
	v_mul_f32_e32 v96, v96, v112
	v_mul_f32_e32 v82, v82, v112
	v_mul_f32_e32 v83, v83, v112
	v_med3_f32 v97, v97, s18, v78
	v_med3_f32 v96, v96, s18, v78
	v_add_f32_e32 v97, 0x4b400000, v97
	v_med3_f32 v82, v82, s18, v78
	v_med3_f32 v83, v83, s18, v78
	v_add_f32_e32 v96, 0x4b400000, v96
	v_add_f32_sdwa v82, v82, s19 dst_sel:WORD_1 dst_unused:UNUSED_PAD src0_sel:DWORD src1_sel:DWORD
	v_add_f32_e32 v83, 0x4b400000, v83
	v_lshlrev_b32_e32 v97, 8, v97
	v_lshl_add_u64 v[110:111], s[94:95], 0, v[66:67]
	v_and_b32_e32 v97, 0xff00, v97
	v_and_b32_e32 v82, 0xff0000, v82
	v_perm_b32 v83, v83, v96, s22
	v_or3_b32 v96, v83, v97, v82
	v_add_co_u32_e32 v82, vcc, s23, v110
	v_mul_f32_e32 v97, v117, v112
	s_nop 0
	v_addc_co_u32_e32 v83, vcc, 0, v111, vcc
	global_store_dword v[82:83], v96, off
	v_mul_f32_e32 v96, v116, v112
	v_mul_f32_e32 v84, v84, v112
	v_mul_f32_e32 v85, v85, v112
	v_med3_f32 v97, v97, s18, v78
	v_med3_f32 v96, v96, s18, v78
	v_add_f32_e32 v97, 0x4b400000, v97
	v_med3_f32 v84, v84, s18, v78
	v_med3_f32 v85, v85, s18, v78
	v_add_f32_e32 v96, 0x4b400000, v96
	v_add_f32_sdwa v84, v84, s19 dst_sel:WORD_1 dst_unused:UNUSED_PAD src0_sel:DWORD src1_sel:DWORD
	v_add_f32_e32 v85, 0x4b400000, v85
	v_lshlrev_b32_e32 v97, 8, v97
	v_and_b32_e32 v97, 0xff00, v97
	v_and_b32_e32 v84, 0xff0000, v84
	v_perm_b32 v85, v85, v96, s22
	v_or3_b32 v84, v85, v97, v84
	v_mul_f32_e32 v85, v101, v112
	global_store_dword v[82:83], v84, off offset:256
	v_mul_f32_e32 v84, v100, v112
	v_mul_f32_e32 v86, v86, v112
	v_mul_f32_e32 v87, v87, v112
	v_med3_f32 v85, v85, s18, v78
	v_med3_f32 v84, v84, s18, v78
	v_add_f32_e32 v85, 0x4b400000, v85
	v_med3_f32 v86, v86, s18, v78
	v_med3_f32 v87, v87, s18, v78
	v_add_f32_e32 v84, 0x4b400000, v84
	v_add_f32_sdwa v86, v86, s19 dst_sel:WORD_1 dst_unused:UNUSED_PAD src0_sel:DWORD src1_sel:DWORD
	v_add_f32_e32 v87, 0x4b400000, v87
	v_lshlrev_b32_e32 v85, 8, v85
	v_and_b32_e32 v85, 0xff00, v85
	v_and_b32_e32 v86, 0xff0000, v86
	v_perm_b32 v84, v87, v84, s22
	v_or3_b32 v84, v84, v85, v86
	v_mul_f32_e32 v85, v105, v112
	global_store_dword v[82:83], v84, off offset:512
	v_mul_f32_e32 v84, v104, v112
	v_mul_f32_e32 v86, v88, v112
	v_mul_f32_e32 v87, v89, v112
	v_med3_f32 v85, v85, s18, v78
	v_med3_f32 v84, v84, s18, v78
	v_add_f32_e32 v85, 0x4b400000, v85
	v_med3_f32 v86, v86, s18, v78
	v_med3_f32 v87, v87, s18, v78
	v_add_f32_e32 v84, 0x4b400000, v84
	v_add_f32_sdwa v86, v86, s19 dst_sel:WORD_1 dst_unused:UNUSED_PAD src0_sel:DWORD src1_sel:DWORD
	v_add_f32_e32 v87, 0x4b400000, v87
	v_lshlrev_b32_e32 v85, 8, v85
	v_and_b32_e32 v85, 0xff00, v85
	v_and_b32_e32 v86, 0xff0000, v86
	v_perm_b32 v84, v87, v84, s22
	v_or3_b32 v84, v84, v85, v86
	v_mul_f32_e32 v85, v99, v112
	global_store_dword v[82:83], v84, off offset:768
	v_mul_f32_e32 v84, v98, v112
	v_mul_f32_e32 v86, v90, v112
	v_mul_f32_e32 v87, v91, v112
	v_med3_f32 v85, v85, s18, v78
	v_med3_f32 v84, v84, s18, v78
	v_add_f32_e32 v85, 0x4b400000, v85
	v_med3_f32 v86, v86, s18, v78
	v_med3_f32 v87, v87, s18, v78
	v_add_f32_e32 v84, 0x4b400000, v84
	v_add_f32_sdwa v86, v86, s19 dst_sel:WORD_1 dst_unused:UNUSED_PAD src0_sel:DWORD src1_sel:DWORD
	v_add_f32_e32 v87, 0x4b400000, v87
	v_lshlrev_b32_e32 v85, 8, v85
	v_and_b32_e32 v85, 0xff00, v85
	v_and_b32_e32 v86, 0xff0000, v86
	v_perm_b32 v84, v87, v84, s22
	v_or3_b32 v84, v84, v85, v86
	v_mul_f32_e32 v85, v107, v112
	global_store_dword v[82:83], v84, off offset:1024
	v_mul_f32_e32 v84, v106, v112
	v_mul_f32_e32 v86, v92, v112
	v_mul_f32_e32 v87, v93, v112
	v_med3_f32 v85, v85, s18, v78
	v_med3_f32 v84, v84, s18, v78
	v_add_f32_e32 v85, 0x4b400000, v85
	v_med3_f32 v86, v86, s18, v78
	v_med3_f32 v87, v87, s18, v78
	v_add_f32_e32 v84, 0x4b400000, v84
	v_add_f32_sdwa v86, v86, s19 dst_sel:WORD_1 dst_unused:UNUSED_PAD src0_sel:DWORD src1_sel:DWORD
	v_add_f32_e32 v87, 0x4b400000, v87
	v_lshlrev_b32_e32 v85, 8, v85
	v_and_b32_e32 v85, 0xff00, v85
	v_and_b32_e32 v86, 0xff0000, v86
	v_perm_b32 v84, v87, v84, s22
	v_or3_b32 v84, v84, v85, v86
	v_mul_f32_e32 v85, v109, v112
	global_store_dword v[82:83], v84, off offset:1280
	v_mul_f32_e32 v84, v108, v112
	v_mul_f32_e32 v86, v94, v112
	v_mul_f32_e32 v87, v95, v112
	v_med3_f32 v85, v85, s18, v78
	v_med3_f32 v84, v84, s18, v78
	v_add_f32_e32 v85, 0x4b400000, v85
	v_med3_f32 v86, v86, s18, v78
	v_med3_f32 v87, v87, s18, v78
	v_add_f32_e32 v84, 0x4b400000, v84
	v_add_f32_sdwa v86, v86, s19 dst_sel:WORD_1 dst_unused:UNUSED_PAD src0_sel:DWORD src1_sel:DWORD
	v_add_f32_e32 v87, 0x4b400000, v87
	v_lshlrev_b32_e32 v85, 8, v85
	v_and_b32_e32 v85, 0xff00, v85
	v_and_b32_e32 v86, 0xff0000, v86
	v_perm_b32 v84, v87, v84, s22
	v_or3_b32 v84, v84, v85, v86
	v_mul_f32_e32 v85, v103, v112
	global_store_dword v[82:83], v84, off offset:1536
	v_mul_f32_e32 v84, v102, v112
	v_mul_f32_e32 v80, v80, v112
	v_mul_f32_e32 v81, v81, v112
	v_med3_f32 v85, v85, s18, v78
	v_med3_f32 v84, v84, s18, v78
	v_add_f32_e32 v85, 0x4b400000, v85
	v_med3_f32 v80, v80, s18, v78
	v_med3_f32 v81, v81, s18, v78
	v_add_f32_e32 v84, 0x4b400000, v84
	v_add_f32_sdwa v80, v80, s19 dst_sel:WORD_1 dst_unused:UNUSED_PAD src0_sel:DWORD src1_sel:DWORD
	v_add_f32_e32 v81, 0x4b400000, v81
	v_lshlrev_b32_e32 v85, 8, v85
	v_and_b32_e32 v85, 0xff00, v85
	v_and_b32_e32 v80, 0xff0000, v80
	v_perm_b32 v81, v81, v84, s22
	v_or3_b32 v80, v81, v85, v80
	global_store_dword v[82:83], v80, off offset:1792
	s_and_saveexec_b64 s[2:3], s[0:1]
	s_cbranch_execz .LBB0_1828
	s_add_u32 s24, s94, s11
	s_addc_u32 s25, s95, s16
	v_mul_f32_e32 v79, 0x3c010204, v79
	global_store_dword v77, v79, s[24:25]
	s_branch .LBB0_1828
